# v54 + write-through (sc1) on the stores of the single-pass phases P0, P3 epilogue, P4, P7 so that the barrier's L2 write-back finds them clean
# speedup vs baseline: 1.0016x; 1.0016x over previous
; DI u32x2 pack4(f32x4 v) { bf16x4_t r = __builtin_convertvector(v, bf16x4_t); return __builtin_bit_cast(u32x2, r); }
; DI void p0_prologue(const Ctx& c) {
;     ...
;     { const f32x4* src = (const f32x4*)kp->in[0]; u32x4* dst = (u32x4*)(c.ws + WS_XB);
;       for (size_t i = gt; i < (size_t)T * D / 8; i += gs) { const f32x4 a = src[2 * i], b = src[2 * i + 1]; const u32x2 lo = pack4(a), hi = pack4(b); dst[i] = (u32x4){lo.x, lo.y, hi.x, hi.y}; } }
.Lp0_unr:
	v_lshl_add_u64 v[96:97], v[8:9], 0, s[14:15]
	v_lshl_add_u64 v[98:99], v[96:97], 0, s[14:15]
	v_lshl_add_u64 v[100:101], v[98:99], 0, s[14:15]
	v_lshl_add_u64 v[102:103], v[100:101], 0, s[14:15]
	v_lshl_add_u64 v[104:105], v[102:103], 0, s[14:15]
	v_lshl_add_u64 v[106:107], v[104:105], 0, s[14:15]
	v_lshl_add_u64 v[108:109], v[106:107], 0, s[14:15]
	global_load_dwordx4 v[32:35], v[8:9], off offset:-16
	global_load_dwordx4 v[36:39], v[8:9], off
	global_load_dwordx4 v[40:43], v[96:97], off offset:-16
	global_load_dwordx4 v[44:47], v[96:97], off
	global_load_dwordx4 v[48:51], v[98:99], off offset:-16
	global_load_dwordx4 v[52:55], v[98:99], off
	global_load_dwordx4 v[56:59], v[100:101], off offset:-16
	global_load_dwordx4 v[60:63], v[100:101], off
	global_load_dwordx4 v[64:67], v[102:103], off offset:-16
	global_load_dwordx4 v[68:71], v[102:103], off
	global_load_dwordx4 v[72:75], v[104:105], off offset:-16
	global_load_dwordx4 v[76:79], v[104:105], off
	global_load_dwordx4 v[80:83], v[106:107], off offset:-16
	global_load_dwordx4 v[84:87], v[106:107], off
	global_load_dwordx4 v[88:91], v[108:109], off offset:-16
	global_load_dwordx4 v[92:95], v[108:109], off
	v_lshl_add_u64 v[8:9], v[108:109], 0, s[14:15]
	v_lshl_add_u64 v[112:113], v[6:7], 0, s[12:13]
	v_lshl_add_u64 v[114:115], v[112:113], 0, s[12:13]
	v_lshl_add_u64 v[116:117], v[114:115], 0, s[12:13]
	v_lshl_add_u64 v[118:119], v[116:117], 0, s[12:13]
	v_lshl_add_u64 v[120:121], v[118:119], 0, s[12:13]
	v_lshl_add_u64 v[122:123], v[120:121], 0, s[12:13]
	v_lshl_add_u64 v[124:125], v[122:123], 0, s[12:13]
	s_waitcnt vmcnt(14)
	v_cvt_pk_bf16_f32 v128, v32, v33
	v_cvt_pk_bf16_f32 v129, v34, v35
	v_cvt_pk_bf16_f32 v130, v36, v37
	v_cvt_pk_bf16_f32 v131, v38, v39
	global_store_dwordx4 v[6:7], v[128:131], off sc1
	s_waitcnt vmcnt(13)
	v_cvt_pk_bf16_f32 v132, v40, v41
	v_cvt_pk_bf16_f32 v133, v42, v43
	v_cvt_pk_bf16_f32 v134, v44, v45
	v_cvt_pk_bf16_f32 v135, v46, v47
	global_store_dwordx4 v[112:113], v[132:135], off sc1
	s_waitcnt vmcnt(12)
	v_cvt_pk_bf16_f32 v136, v48, v49
	v_cvt_pk_bf16_f32 v137, v50, v51
	v_cvt_pk_bf16_f32 v138, v52, v53
	v_cvt_pk_bf16_f32 v139, v54, v55
	global_store_dwordx4 v[114:115], v[136:139], off sc1
	s_waitcnt vmcnt(11)
	v_cvt_pk_bf16_f32 v140, v56, v57
	v_cvt_pk_bf16_f32 v141, v58, v59
	v_cvt_pk_bf16_f32 v142, v60, v61
	v_cvt_pk_bf16_f32 v143, v62, v63
	global_store_dwordx4 v[116:117], v[140:143], off sc1
	s_waitcnt vmcnt(10)
	v_cvt_pk_bf16_f32 v144, v64, v65
	v_cvt_pk_bf16_f32 v145, v66, v67
	v_cvt_pk_bf16_f32 v146, v68, v69
	v_cvt_pk_bf16_f32 v147, v70, v71
	global_store_dwordx4 v[118:119], v[144:147], off sc1
	s_waitcnt vmcnt(9)
	v_cvt_pk_bf16_f32 v148, v72, v73
	v_cvt_pk_bf16_f32 v149, v74, v75
	v_cvt_pk_bf16_f32 v150, v76, v77
	v_cvt_pk_bf16_f32 v151, v78, v79
	global_store_dwordx4 v[120:121], v[148:151], off sc1
	s_waitcnt vmcnt(8)
	v_cvt_pk_bf16_f32 v152, v80, v81
	v_cvt_pk_bf16_f32 v153, v82, v83
	v_cvt_pk_bf16_f32 v154, v84, v85
	v_cvt_pk_bf16_f32 v155, v86, v87
	global_store_dwordx4 v[122:123], v[152:155], off sc1
	s_waitcnt vmcnt(7)
	v_cvt_pk_bf16_f32 v156, v88, v89
	v_cvt_pk_bf16_f32 v157, v90, v91
	v_cvt_pk_bf16_f32 v158, v92, v93
	v_cvt_pk_bf16_f32 v159, v94, v95
	global_store_dwordx4 v[124:125], v[156:159], off sc1
	v_lshl_add_u64 v[6:7], v[124:125], 0, s[12:13]
	s_sub_i32 s98, s98, 1
	s_cmp_lg_u32 s98, 0
	s_cbranch_scc1 .Lp0_unr
	s_branch .LBB0_8
.LBB0_7:
	global_load_dwordx4 v[14:17], v[8:9], off offset:-16
	global_load_dwordx4 v[18:21], v[8:9], off
	v_lshl_add_u64 v[10:11], v[10:11], 0, s[6:7]
	v_cmp_lt_u64_e32 vcc, s[18:19], v[10:11]
	v_lshl_add_u64 v[8:9], v[8:9], 0, s[14:15]
	s_or_b64 s[16:17], vcc, s[16:17]
	s_waitcnt vmcnt(1)
	v_cvt_pk_bf16_f32 v23, v16, v17
	v_cvt_pk_bf16_f32 v22, v14, v15
	s_waitcnt vmcnt(0)
	v_cvt_pk_bf16_f32 v25, v20, v21
	v_cvt_pk_bf16_f32 v24, v18, v19
	global_store_dwordx4 v[6:7], v[22:25], off sc1
	v_lshl_add_u64 v[6:7], v[6:7], 0, s[12:13]
	s_andn2_b64 exec, exec, s[16:17]
	s_cbranch_execnz .LBB0_7

; DI u32x2 pack4(f32x4 v) { bf16x4_t r = __builtin_convertvector(v, bf16x4_t); return __builtin_bit_cast(u32x2, r); }
; DI void p0_prologue(const Ctx& c) {
;     ...
;     { const f32x4* src = (const f32x4*)kp->in[1]; u32x4* dst = (u32x4*)(c.ws + WS_PB);
;       for (size_t i = gt; i < (size_t)T * PLE / 8; i += gs) { const f32x4 a = src[2 * i], b = src[2 * i + 1]; const u32x2 lo = pack4(a), hi = pack4(b); dst[i] = (u32x4){lo.x, lo.y, hi.x, hi.y}; } }
.LBB0_10:
	global_load_dwordx4 v[14:17], v[4:5], off offset:-16
	global_load_dwordx4 v[18:21], v[4:5], off
	v_lshl_add_u64 v[8:9], v[8:9], 0, s[6:7]
	v_cmp_lt_u64_e32 vcc, s[16:17], v[8:9]
	v_lshl_add_u64 v[4:5], v[4:5], 0, s[12:13]
	s_or_b64 s[14:15], vcc, s[14:15]
	s_waitcnt vmcnt(1)
	v_cvt_pk_bf16_f32 v23, v16, v17
	v_cvt_pk_bf16_f32 v22, v14, v15
	s_waitcnt vmcnt(0)
	v_cvt_pk_bf16_f32 v25, v20, v21
	v_cvt_pk_bf16_f32 v24, v18, v19
	global_store_dwordx4 v[6:7], v[22:25], off sc1
	v_lshl_add_u64 v[6:7], v[6:7], 0, s[8:9]
	s_andn2_b64 exec, exec, s[14:15]
	s_cbranch_execnz .LBB0_10

; DI void p0_prologue(const Ctx& c) {
;     ...
;     { f32x2* rope = (f32x2*)(c.ws + WS_ROPE);
;       for (size_t i = gt; i < (size_t)SEQ * 64; i += gs) { const int pos = (int)(i >> 6), k = (int)(i & 63);
;         const float inv = exp2f(-(float)k * (13.287712379549449f / 64.0f));
;         const float ang = (float)pos * inv;
;         double rv = (double)ang * 0.15915494309189535; rv -= floor(rv);
;         const float f = (float)rv;
;         rope[i] = (f32x2){__builtin_amdgcn_cosf(f), __builtin_amdgcn_sinf(f)}; } }
.LBB0_13:
	v_lshrrev_b64 v[6:7], 6, v[0:1]
	v_ffbh_u32_e32 v5, v7
	v_min_u32_e32 v5, 32, v5
	v_lshlrev_b64 v[6:7], v5, v[6:7]
	v_min_u32_e32 v6, 1, v6
	v_or_b32_e32 v6, v7, v6
	v_cvt_f32_u32_e32 v6, v6
	v_sub_u32_e32 v5, 32, v5
	v_lshl_add_u64 v[0:1], v[0:1], 0, s[6:7]
	v_cmp_lt_u64_e32 vcc, s[16:17], v[0:1]
	v_ldexp_f32 v5, v6, v5
	v_mul_f32_e32 v5, v4, v5
	v_cvt_f64_f32_e32 v[6:7], v5
	v_mul_f64 v[8:9], v[6:7], s[14:15]
	v_floor_f64_e32 v[8:9], v[8:9]
	v_fma_f64 v[6:7], v[6:7], s[14:15], -v[8:9]
	v_cvt_f32_f64_e32 v5, v[6:7]
	v_cos_f32_e32 v6, v5
	v_sin_f32_e32 v7, v5
	s_or_b64 s[12:13], vcc, s[12:13]
	global_store_dwordx2 v[2:3], v[6:7], off sc1
	v_lshl_add_u64 v[2:3], v[2:3], 0, s[10:11]
	s_andn2_b64 exec, exec, s[12:13]
	s_cbranch_execnz .LBB0_13

; #define G_SETUP_B(u) do { rsB0 = mk_rsrc((u).b0); rsB1 = mk_rsrc((u).b1); } while (0)
;     ...
;         U nxt = cur;
;         const bool has_next = sched.get(ui + 1, nxt);
;         G_SETUP_B(nxt);
;         G_TILE(G_A0, G_B0, true, G_B1, G_A1, nt - 1, true, 0, G_SETUP_A(nxt));
.LBB0_375:
	s_mov_b32 m0, s72
	ds_read_b64_tr_b16 v[170:171], v165
	ds_read_b64_tr_b16 v[174:175], v165 offset:32
	ds_read_b64_tr_b16 v[178:179], v165 offset:64
	ds_read_b64_tr_b16 v[182:183], v165 offset:96
	ds_read_b64_tr_b16 v[172:173], v166
	ds_read_b64_tr_b16 v[176:177], v166 offset:32
	ds_read_b64_tr_b16 v[180:181], v166 offset:64
	ds_read_b64_tr_b16 v[184:185], v166 offset:96
	ds_read_b128 v[186:189], v162
	ds_read_b128 v[190:193], v162 offset:2048
	ds_read_b128 v[198:201], v162 offset:4096
	buffer_load_dwordx4 v163, s[20:23], s73 offen lds
	s_mov_b32 m0, s71
	s_and_b32 s17, s53, 0xffff
	buffer_load_dwordx4 v164, s[20:23], s73 offen lds
	s_mov_b32 m0, s70
	s_and_b32 s13, s48, 0xffff
	buffer_load_dwordx4 v167, s[20:23], s73 offen lds
	s_mov_b32 m0, s68
	s_mov_b32 s12, s47
	buffer_load_dwordx4 v168, s[20:23], s73 offen lds
	v_mbcnt_lo_u32_b32 v163, -1, 0
	v_mbcnt_hi_u32_b32 v163, -1, v163
	s_mov_b32 s16, s49
	v_lshlrev_b32_e32 v164, 4, v163
	v_and_b32_e32 v167, 32, v163
	v_lshrrev_b32_e32 v163, 2, v163
	v_bitop3_b32 v164, v164, v167, 48 bitop3:0x6c
	v_add_lshl_u32 v163, v163, s54, 12
	v_or3_b32 v163, v164, s55, v163
	s_mov_b32 s20, s49
	s_mov_b32 s21, s17
	s_mov_b32 s22, s10
	s_mov_b32 s23, s11
	s_and_b32 s19, s46, 0xffff
	s_mov_b32 s18, s43
	v_add_u32_e32 v164, 0x40000, v163
	v_add_u32_e32 v167, 0x80000, v163
	v_add_u32_e32 v168, 0xc0000, v163
	s_mov_b32 s8, s47
	s_mov_b32 s9, s13
	s_mov_b32 s24, s43
	s_mov_b32 s25, s19
	s_mov_b32 s26, s10
	s_mov_b32 s27, s11
	s_waitcnt lgkmcnt(2)
	v_mfma_f32_16x16x32_bf16 v[156:159], v[170:173], v[186:189], v[156:159]
	v_mfma_f32_16x16x32_bf16 v[152:155], v[174:177], v[186:189], v[152:155]
	v_mfma_f32_16x16x32_bf16 v[148:151], v[178:181], v[186:189], v[148:151]
	v_mfma_f32_16x16x32_bf16 v[144:147], v[182:185], v[186:189], v[144:147]
	s_waitcnt vmcnt(11)
	v_cvt_pk_bf16_f32 v15, v14, v15
	v_cvt_pk_bf16_f32 v14, v12, v13
	ds_read_b128 v[186:189], v162 offset:6144
	ds_write_b64 v161, v[14:15] offset:34816
	s_waitcnt lgkmcnt(3)
	v_mfma_f32_16x16x32_bf16 v[12:15], v[182:185], v[190:193], v[128:131]
	v_mfma_f32_16x16x32_bf16 v[140:143], v[170:173], v[190:193], v[140:143]
	v_mfma_f32_16x16x32_bf16 v[136:139], v[174:177], v[190:193], v[136:139]
	v_mfma_f32_16x16x32_bf16 v[132:135], v[178:181], v[190:193], v[132:135]
	buffer_load_dwordx4 v[128:131], v160, s[8:11], 0 offen
	ds_read_b128 v[190:193], v162 offset:8192
	s_waitcnt lgkmcnt(3)
	v_mfma_f32_16x16x32_bf16 v[124:127], v[170:173], v[198:201], v[124:127]
	v_mfma_f32_16x16x32_bf16 v[120:123], v[174:177], v[198:201], v[120:123]
	v_mfma_f32_16x16x32_bf16 v[116:119], v[178:181], v[198:201], v[116:119]
	v_mfma_f32_16x16x32_bf16 v[112:115], v[182:185], v[198:201], v[112:115]
	s_waitcnt vmcnt(10)
	v_cvt_pk_bf16_f32 v31, v30, v31
	v_cvt_pk_bf16_f32 v30, v28, v29
	ds_read_b128 v[198:201], v162 offset:10240
	ds_write_b64 v161, v[30:31] offset:43520
	s_waitcnt lgkmcnt(4)
	v_mfma_f32_16x16x32_bf16 v[28:31], v[182:185], v[186:189], v[96:99]
	v_mfma_f32_16x16x32_bf16 v[108:111], v[170:173], v[186:189], v[108:111]
	v_mfma_f32_16x16x32_bf16 v[104:107], v[174:177], v[186:189], v[104:107]
	v_mfma_f32_16x16x32_bf16 v[100:103], v[178:181], v[186:189], v[100:103]
	buffer_load_dwordx4 v[96:99], v160, s[8:11], s11 offen
	ds_read_b128 v[186:189], v162 offset:12288
	s_waitcnt lgkmcnt(3)
	v_mfma_f32_16x16x32_bf16 v[92:95], v[170:173], v[190:193], v[92:95]
	v_mfma_f32_16x16x32_bf16 v[88:91], v[174:177], v[190:193], v[88:91]
	v_mfma_f32_16x16x32_bf16 v[84:87], v[178:181], v[190:193], v[84:87]
	v_mfma_f32_16x16x32_bf16 v[80:83], v[182:185], v[190:193], v[80:83]
	v_cvt_pk_bf16_f32 v7, v6, v7
	v_cvt_pk_bf16_f32 v6, v4, v5
	ds_read_b128 v[190:193], v162 offset:14336
	ds_write_b64 v161, v[6:7] offset:52224
	s_waitcnt lgkmcnt(4)
	v_mfma_f32_16x16x32_bf16 v[4:7], v[182:185], v[198:201], v[64:67]
	v_mfma_f32_16x16x32_bf16 v[76:79], v[170:173], v[198:201], v[76:79]
	v_mfma_f32_16x16x32_bf16 v[72:75], v[174:177], v[198:201], v[72:75]
	v_mfma_f32_16x16x32_bf16 v[68:71], v[178:181], v[198:201], v[68:71]
	buffer_load_dwordx4 v[64:67], v160, s[8:11], s56 offen
	ds_read_b128 v[198:201], v162 offset:1024
	s_waitcnt lgkmcnt(3)
	v_mfma_f32_16x16x32_bf16 v[60:63], v[170:173], v[186:189], v[60:63]
	v_mfma_f32_16x16x32_bf16 v[56:59], v[174:177], v[186:189], v[56:59]
	v_mfma_f32_16x16x32_bf16 v[52:55], v[178:181], v[186:189], v[52:55]
	v_mfma_f32_16x16x32_bf16 v[48:51], v[182:185], v[186:189], v[48:51]
	s_waitcnt lgkmcnt(2)
	v_mfma_f32_16x16x32_bf16 v[44:47], v[170:173], v[190:193], v[44:47]
	ds_read_b128 v[170:173], v162 offset:3072
	v_mfma_f32_16x16x32_bf16 v[40:43], v[174:177], v[190:193], v[40:43]
	ds_read_b64_tr_b16 v[174:175], v165 offset:17408
	ds_read_b64_tr_b16 v[186:187], v165 offset:17440
	ds_read_b64_tr_b16 v[202:203], v165 offset:17472
	ds_read_b64_tr_b16 v[206:207], v165 offset:17504
	ds_read_b64_tr_b16 v[176:177], v166 offset:17408
	ds_read_b64_tr_b16 v[188:189], v166 offset:17440
	ds_read_b64_tr_b16 v[204:205], v166 offset:17472
	ds_read_b64_tr_b16 v[208:209], v166 offset:17504
	v_mfma_f32_16x16x32_bf16 v[36:39], v[178:181], v[190:193], v[36:39]
	s_waitcnt vmcnt(11)
	v_cvt_pk_bf16_f32 v179, v26, v27
	v_cvt_pk_bf16_f32 v178, v24, v25
	ds_write_b64 v161, v[178:179] offset:60928
	v_mfma_f32_16x16x32_bf16 v[24:27], v[182:185], v[190:193], v[32:35]
	s_nop 2
	buffer_load_dwordx4 v[32:35], v160, s[8:11], s57 offen
	ds_read_b128 v[178:181], v162 offset:5120
	s_waitcnt lgkmcnt(5)
	v_mfma_f32_16x16x32_bf16 v[156:159], v[174:177], v[198:201], v[156:159]
	s_waitcnt lgkmcnt(4)
	v_mfma_f32_16x16x32_bf16 v[152:155], v[186:189], v[198:201], v[152:155]
	s_waitcnt lgkmcnt(3)
; #define G_ENDTILE(VM) do { asm volatile("s_waitcnt vmcnt(" #VM ")" ::: "memory"); \
;         asm volatile("s_waitcnt lgkmcnt(0)" ::: "memory"); __builtin_amdgcn_s_barrier(); asm volatile("" ::: "memory"); } while (0)
;     ...
;         G_TILE(G_A0, G_B0, true, G_B1, G_A1, nt - 1, true, 0, G_SETUP_A(nxt));
;         G_ENDTILE(8);
;         G_TILE(G_A1, G_B1, true, G_B0, G_A0, 0, true, 1, (void)0);
	v_mfma_f32_16x16x32_bf16 v[148:151], v[202:205], v[198:201], v[148:151]
	s_waitcnt lgkmcnt(2)
	v_mfma_f32_16x16x32_bf16 v[144:147], v[206:209], v[198:201], v[144:147]
	ds_read_b128 v[182:185], v162 offset:7168
	v_mfma_f32_16x16x32_bf16 v[12:15], v[206:209], v[170:173], v[12:15]
	s_waitcnt vmcnt(11)
	v_cvt_pk_bf16_f32 v23, v22, v23
	v_cvt_pk_bf16_f32 v22, v20, v21
	ds_write_b64 v161, v[22:23] offset:35072
	v_mfma_f32_16x16x32_bf16 v[140:143], v[174:177], v[170:173], v[140:143]
	v_mfma_f32_16x16x32_bf16 v[136:139], v[186:189], v[170:173], v[136:139]
	v_mfma_f32_16x16x32_bf16 v[132:135], v[202:205], v[170:173], v[132:135]
	buffer_load_dwordx4 v[20:23], v160, s[20:23], 0 offen
	ds_read_b128 v[170:173], v162 offset:9216
	s_waitcnt lgkmcnt(3)
	v_mfma_f32_16x16x32_bf16 v[124:127], v[174:177], v[178:181], v[124:127]
	v_mfma_f32_16x16x32_bf16 v[120:123], v[186:189], v[178:181], v[120:123]
	v_mfma_f32_16x16x32_bf16 v[116:119], v[202:205], v[178:181], v[116:119]
	v_mfma_f32_16x16x32_bf16 v[112:115], v[206:209], v[178:181], v[112:115]
	s_waitcnt vmcnt(10)
	v_cvt_pk_bf16_f32 v11, v10, v11
	v_cvt_pk_bf16_f32 v10, v8, v9
	ds_read_b128 v[178:181], v162 offset:11264
	ds_write_b64 v161, v[10:11] offset:43776
	s_waitcnt lgkmcnt(4)
	v_mfma_f32_16x16x32_bf16 v[8:11], v[206:209], v[182:185], v[28:31]
	v_mfma_f32_16x16x32_bf16 v[108:111], v[174:177], v[182:185], v[108:111]
	v_mfma_f32_16x16x32_bf16 v[104:107], v[186:189], v[182:185], v[104:107]
	v_mfma_f32_16x16x32_bf16 v[100:103], v[202:205], v[182:185], v[100:103]
	buffer_load_dwordx4 v[182:185], v160, s[20:23], s11 offen
	ds_read_b128 v[28:31], v162 offset:13312
	s_waitcnt lgkmcnt(3)
	v_mfma_f32_16x16x32_bf16 v[92:95], v[174:177], v[170:173], v[92:95]
	v_mfma_f32_16x16x32_bf16 v[88:91], v[186:189], v[170:173], v[88:91]
	v_mfma_f32_16x16x32_bf16 v[84:87], v[202:205], v[170:173], v[84:87]
	v_mfma_f32_16x16x32_bf16 v[80:83], v[206:209], v[170:173], v[80:83]
	v_cvt_pk_bf16_f32 v3, v2, v3
	v_cvt_pk_bf16_f32 v2, v0, v1
	ds_read_b128 v[170:173], v162 offset:15360
	ds_write_b64 v161, v[2:3] offset:52480
	s_waitcnt lgkmcnt(4)
	v_mfma_f32_16x16x32_bf16 v[0:3], v[206:209], v[178:181], v[4:7]
	v_mfma_f32_16x16x32_bf16 v[76:79], v[174:177], v[178:181], v[76:79]
	v_mfma_f32_16x16x32_bf16 v[72:75], v[186:189], v[178:181], v[72:75]
	v_mfma_f32_16x16x32_bf16 v[68:71], v[202:205], v[178:181], v[68:71]
	buffer_load_dwordx4 v[178:181], v160, s[20:23], s56 offen
	s_waitcnt lgkmcnt(2)
	v_mfma_f32_16x16x32_bf16 v[60:63], v[174:177], v[28:31], v[60:63]
	v_mfma_f32_16x16x32_bf16 v[56:59], v[186:189], v[28:31], v[56:59]
	v_mfma_f32_16x16x32_bf16 v[52:55], v[202:205], v[28:31], v[52:55]
	v_mfma_f32_16x16x32_bf16 v[48:51], v[206:209], v[28:31], v[48:51]
	s_waitcnt vmcnt(11)
	v_cvt_pk_bf16_f32 v5, v18, v19
	v_cvt_pk_bf16_f32 v4, v16, v17
	s_waitcnt lgkmcnt(1)
	v_mfma_f32_16x16x32_bf16 v[16:19], v[206:209], v[170:173], v[24:27]
	ds_write_b64 v161, v[4:5] offset:61184
	v_mfma_f32_16x16x32_bf16 v[44:47], v[174:177], v[170:173], v[44:47]
	v_mfma_f32_16x16x32_bf16 v[40:43], v[186:189], v[170:173], v[40:43]
	v_mfma_f32_16x16x32_bf16 v[36:39], v[202:205], v[170:173], v[36:39]
	buffer_load_dwordx4 v[170:173], v160, s[20:23], s57 offen
	s_waitcnt vmcnt(8)
	s_mov_b32 m0, s59
	s_waitcnt lgkmcnt(0)
	s_barrier
	ds_read_b64_tr_b16 v[24:25], v165 offset:34816
	ds_read_b64_tr_b16 v[26:27], v166 offset:34816
	ds_read_b64_tr_b16 v[176:177], v166 offset:34848
	ds_read_b128 v[4:7], v162 offset:32768
	ds_read_b64_tr_b16 v[174:175], v165 offset:34848
	ds_read_b64_tr_b16 v[186:187], v165 offset:34880
	ds_read_b64_tr_b16 v[190:191], v165 offset:34912
	ds_read_b64_tr_b16 v[188:189], v166 offset:34880
	ds_read_b64_tr_b16 v[192:193], v166 offset:34912
	ds_read_b128 v[28:31], v162 offset:34816
	ds_read_b128 v[198:201], v162 offset:36864
	buffer_load_dwordx4 v163, s[24:27], 0 offen lds
	s_mov_b32 m0, s60
	s_waitcnt lgkmcnt(7)
	v_mfma_f32_16x16x32_bf16 v[156:159], v[24:27], v[4:7], v[156:159]
	buffer_load_dwordx4 v164, s[24:27], 0 offen lds
	s_mov_b32 m0, s61
	s_nop 0
	buffer_load_dwordx4 v167, s[24:27], 0 offen lds
	s_mov_b32 m0, s62
	s_waitcnt lgkmcnt(6)
	v_mfma_f32_16x16x32_bf16 v[152:155], v[174:177], v[4:7], v[152:155]
	buffer_load_dwordx4 v168, s[24:27], 0 offen lds
	s_waitcnt lgkmcnt(3)
	v_mfma_f32_16x16x32_bf16 v[148:151], v[186:189], v[4:7], v[148:151]
	s_waitcnt lgkmcnt(2)
	v_mfma_f32_16x16x32_bf16 v[144:147], v[190:193], v[4:7], v[144:147]
	ds_read_b128 v[4:7], v162 offset:38912
	s_waitcnt vmcnt(11)
	v_cvt_pk_bf16_f32 v131, v130, v131
	v_cvt_pk_bf16_f32 v130, v128, v129
	s_waitcnt lgkmcnt(2)
	v_mfma_f32_16x16x32_bf16 v[140:143], v[24:27], v[28:31], v[140:143]
	ds_write_b64 v161, v[130:131]
	v_mfma_f32_16x16x32_bf16 v[202:205], v[174:177], v[28:31], v[136:139]
	v_mfma_f32_16x16x32_bf16 v[132:135], v[186:189], v[28:31], v[132:135]
	v_mfma_f32_16x16x32_bf16 v[206:209], v[190:193], v[28:31], v[12:15]
	s_nop 2
	buffer_load_dwordx4 v[12:15], v160, s[8:11], s63 offen
	ds_read_b128 v[128:131], v162 offset:40960
	s_waitcnt lgkmcnt(3)
	v_mfma_f32_16x16x32_bf16 v[124:127], v[24:27], v[198:201], v[124:127]
	v_mfma_f32_16x16x32_bf16 v[120:123], v[174:177], v[198:201], v[120:123]
	v_mfma_f32_16x16x32_bf16 v[116:119], v[186:189], v[198:201], v[116:119]
	v_mfma_f32_16x16x32_bf16 v[198:201], v[190:193], v[198:201], v[112:115]
	s_waitcnt lgkmcnt(2)
	v_mfma_f32_16x16x32_bf16 v[210:213], v[174:177], v[4:7], v[104:107]
	s_waitcnt vmcnt(11)
; #define G_ENDTILE(VM) do { asm volatile("s_waitcnt vmcnt(" #VM ")" ::: "memory"); \
;         asm volatile("s_waitcnt lgkmcnt(0)" ::: "memory"); __builtin_amdgcn_s_barrier(); asm volatile("" ::: "memory"); } while (0)
;     ...
;         G_TILE(G_A1, G_B1, true, G_B0, G_A0, 0, true, 1, (void)0);
;         G_ENDTILE(8);
	v_cvt_pk_bf16_f32 v29, v98, v99
	v_cvt_pk_bf16_f32 v28, v96, v97
	ds_read_b128 v[104:107], v162 offset:43008
	v_mfma_f32_16x16x32_bf16 v[8:11], v[190:193], v[4:7], v[8:11]
	ds_write_b64 v161, v[28:29] offset:8704
	v_mfma_f32_16x16x32_bf16 v[108:111], v[24:27], v[4:7], v[108:111]
	v_mfma_f32_16x16x32_bf16 v[100:103], v[186:189], v[4:7], v[100:103]
	buffer_load_dwordx4 v[28:31], v160, s[8:11], s65 offen
	ds_read_b128 v[96:99], v162 offset:45056
	s_waitcnt lgkmcnt(3)
	v_mfma_f32_16x16x32_bf16 v[92:95], v[24:27], v[128:131], v[92:95]
	v_mfma_f32_16x16x32_bf16 v[88:91], v[174:177], v[128:131], v[88:91]
	v_mfma_f32_16x16x32_bf16 v[84:87], v[186:189], v[128:131], v[84:87]
	v_mfma_f32_16x16x32_bf16 v[214:217], v[190:193], v[128:131], v[80:83]
	s_waitcnt lgkmcnt(2)
	v_mfma_f32_16x16x32_bf16 v[218:221], v[174:177], v[104:107], v[72:75]
	s_waitcnt vmcnt(11)
	v_cvt_pk_bf16_f32 v5, v66, v67
	v_cvt_pk_bf16_f32 v4, v64, v65
	ds_read_b128 v[72:75], v162 offset:47104
	v_mfma_f32_16x16x32_bf16 v[0:3], v[190:193], v[104:107], v[0:3]
	ds_write_b64 v161, v[4:5] offset:17408
	v_mfma_f32_16x16x32_bf16 v[76:79], v[24:27], v[104:107], v[76:79]
	v_mfma_f32_16x16x32_bf16 v[68:71], v[186:189], v[104:107], v[68:71]
	buffer_load_dwordx4 v[4:7], v160, s[8:11], s64 offen
	ds_read_b128 v[64:67], v162 offset:33792
	s_waitcnt lgkmcnt(3)
	v_mfma_f32_16x16x32_bf16 v[60:63], v[24:27], v[96:99], v[60:63]
	v_mfma_f32_16x16x32_bf16 v[56:59], v[174:177], v[96:99], v[56:59]
	v_mfma_f32_16x16x32_bf16 v[52:55], v[186:189], v[96:99], v[52:55]
	v_mfma_f32_16x16x32_bf16 v[48:51], v[190:193], v[96:99], v[48:51]
	ds_read_b128 v[80:83], v162 offset:35840
	s_waitcnt lgkmcnt(3)
	v_mfma_f32_16x16x32_bf16 v[174:177], v[174:177], v[72:75], v[40:43]
	s_nop 2
	ds_read_b64_tr_b16 v[40:41], v165 offset:52224
	ds_read_b64_tr_b16 v[222:223], v165 offset:52256
	ds_read_b64_tr_b16 v[226:227], v165 offset:52288
	ds_read_b64_tr_b16 v[230:231], v165 offset:52320
	ds_read_b64_tr_b16 v[42:43], v166 offset:52224
	ds_read_b64_tr_b16 v[224:225], v166 offset:52256
	ds_read_b64_tr_b16 v[228:229], v166 offset:52288
	ds_read_b64_tr_b16 v[232:233], v166 offset:52320
	v_mfma_f32_16x16x32_bf16 v[16:19], v[190:193], v[72:75], v[16:19]
	v_mfma_f32_16x16x32_bf16 v[44:47], v[24:27], v[72:75], v[44:47]
	s_waitcnt vmcnt(11)
	v_cvt_pk_bf16_f32 v25, v34, v35
	v_cvt_pk_bf16_f32 v24, v32, v33
	ds_write_b64 v161, v[24:25] offset:26112
	v_mfma_f32_16x16x32_bf16 v[186:189], v[186:189], v[72:75], v[36:39]
	buffer_load_dwordx4 v[24:27], v160, s[8:11], s66 offen
	ds_read_b128 v[32:35], v162 offset:37888
	s_waitcnt lgkmcnt(5)
	v_mfma_f32_16x16x32_bf16 v[156:159], v[40:43], v[64:67], v[156:159]
	s_waitcnt lgkmcnt(4)
	v_mfma_f32_16x16x32_bf16 v[152:155], v[222:225], v[64:67], v[152:155]
	s_waitcnt lgkmcnt(3)
	v_mfma_f32_16x16x32_bf16 v[148:151], v[226:229], v[64:67], v[148:151]
	s_waitcnt lgkmcnt(2)
	v_mfma_f32_16x16x32_bf16 v[190:193], v[230:233], v[64:67], v[144:147]
	ds_read_b128 v[36:39], v162 offset:39936
	s_waitcnt vmcnt(11)
	v_cvt_pk_bf16_f32 v23, v22, v23
	v_cvt_pk_bf16_f32 v22, v20, v21
	v_mfma_f32_16x16x32_bf16 v[136:139], v[40:43], v[80:83], v[140:143]
	ds_write_b64 v161, v[22:23] offset:256
	v_mfma_f32_16x16x32_bf16 v[128:131], v[222:225], v[80:83], v[202:205]
	v_mfma_f32_16x16x32_bf16 v[132:135], v[226:229], v[80:83], v[132:135]
	v_mfma_f32_16x16x32_bf16 v[140:143], v[230:233], v[80:83], v[206:209]
	buffer_load_dwordx4 v[20:23], v160, s[20:23], s63 offen
	ds_read_b128 v[64:67], v162 offset:41984
	s_waitcnt lgkmcnt(3)
	v_mfma_f32_16x16x32_bf16 v[124:127], v[40:43], v[32:35], v[124:127]
	v_mfma_f32_16x16x32_bf16 v[120:123], v[222:225], v[32:35], v[120:123]
	v_mfma_f32_16x16x32_bf16 v[112:115], v[226:229], v[32:35], v[116:119]
	v_mfma_f32_16x16x32_bf16 v[116:119], v[230:233], v[32:35], v[198:201]
	ds_read_b128 v[32:35], v162 offset:44032
	s_waitcnt vmcnt(11)
	v_cvt_pk_bf16_f32 v73, v184, v185
	v_cvt_pk_bf16_f32 v72, v182, v183
	s_waitcnt lgkmcnt(3)
	v_mfma_f32_16x16x32_bf16 v[104:107], v[40:43], v[36:39], v[108:111]
	ds_write_b64 v161, v[72:73] offset:8960
	v_mfma_f32_16x16x32_bf16 v[96:99], v[222:225], v[36:39], v[210:213]
	v_mfma_f32_16x16x32_bf16 v[100:103], v[226:229], v[36:39], v[100:103]
	v_mfma_f32_16x16x32_bf16 v[108:111], v[230:233], v[36:39], v[8:11]
	s_nop 2
	buffer_load_dwordx4 v[8:11], v160, s[20:23], s65 offen
	ds_read_b128 v[36:39], v162 offset:46080
	s_waitcnt lgkmcnt(3)
	v_mfma_f32_16x16x32_bf16 v[92:95], v[40:43], v[64:67], v[92:95]
	v_mfma_f32_16x16x32_bf16 v[88:91], v[222:225], v[64:67], v[88:91]
	v_mfma_f32_16x16x32_bf16 v[80:83], v[226:229], v[64:67], v[84:87]
	v_mfma_f32_16x16x32_bf16 v[84:87], v[230:233], v[64:67], v[214:217]
	ds_read_b128 v[144:147], v162 offset:48128
	s_waitcnt lgkmcnt(3)
	v_mfma_f32_16x16x32_bf16 v[72:75], v[40:43], v[32:35], v[76:79]
	s_waitcnt vmcnt(11)
	s_nop 1
	v_cvt_pk_bf16_f32 v77, v180, v181
	v_cvt_pk_bf16_f32 v76, v178, v179
	v_mfma_f32_16x16x32_bf16 v[64:67], v[222:225], v[32:35], v[218:221]
	ds_write_b64 v161, v[76:77] offset:17664
	v_mfma_f32_16x16x32_bf16 v[68:71], v[226:229], v[32:35], v[68:71]
	v_mfma_f32_16x16x32_bf16 v[76:79], v[230:233], v[32:35], v[0:3]
	s_nop 2
	buffer_load_dwordx4 v[0:3], v160, s[20:23], s64 offen
	s_waitcnt lgkmcnt(2)
	v_mfma_f32_16x16x32_bf16 v[60:63], v[40:43], v[36:39], v[60:63]
	v_mfma_f32_16x16x32_bf16 v[56:59], v[222:225], v[36:39], v[56:59]
	v_mfma_f32_16x16x32_bf16 v[52:55], v[226:229], v[36:39], v[52:55]
	v_mfma_f32_16x16x32_bf16 v[48:51], v[230:233], v[36:39], v[48:51]
	s_waitcnt lgkmcnt(1)
	v_mfma_f32_16x16x32_bf16 v[40:43], v[40:43], v[144:147], v[44:47]
	s_waitcnt vmcnt(11)
	s_nop 1
	v_cvt_pk_bf16_f32 v45, v172, v173
	v_cvt_pk_bf16_f32 v44, v170, v171
	v_mfma_f32_16x16x32_bf16 v[36:39], v[222:225], v[144:147], v[174:177]
	ds_write_b64 v161, v[44:45] offset:26368
	v_mfma_f32_16x16x32_bf16 v[32:35], v[226:229], v[144:147], v[186:189]
	v_mfma_f32_16x16x32_bf16 v[44:47], v[230:233], v[144:147], v[16:19]
	s_nop 2
	buffer_load_dwordx4 v[16:19], v160, s[20:23], s66 offen
	s_waitcnt vmcnt(8)
	s_waitcnt lgkmcnt(0)
	s_barrier
	s_mov_b32 s100, 0x10000
	s_mov_b32 s101, 0
	v_mbcnt_lo_u32_b32 v144, -1, 0
	v_mbcnt_hi_u32_b32 v144, -1, v144
	s_and_b64 vcc, exec, s[14:15]
	v_and_or_b32 v145, v144, 15, s74
	v_ashrrev_i32_e32 v144, 1, v144
	v_and_b32_e32 v146, -8, v144
	v_add_u32_e32 v144, s51, v145
	s_ashr_i32 s51, s50, 31
	v_ashrrev_i32_e32 v147, 31, v146
	v_ashrrev_i32_e32 v145, 31, v144
	s_or_b64 s[8:9], s[50:51], s[28:29]
	v_lshlrev_b64 v[170:171], 11, v[144:145]
	v_lshl_add_u64 v[146:147], s[8:9], 0, v[146:147]
	v_lshl_add_u64 v[170:171], v[170:171], 0, v[146:147]
	v_lshlrev_b64 v[178:179], 1, v[170:171]
	v_lshl_add_u64 v[174:175], s[36:37], 0, v[178:179]
	v_mov_b32_e32 v198, v174
	v_mov_b32_e32 v199, v175
	global_load_dwordx4 v[170:173], v[174:175], off
	s_nop 0
	global_load_dwordx4 v[174:177], v[174:175], off offset:64
	v_lshl_add_u64 v[198:199], v[198:199], 0, s[100:101]
	global_load_dwordx4 v[208:211], v[198:199], off
	global_load_dwordx4 v[212:215], v[198:199], off offset:64
	v_add_u32_e32 v180, 16, v144
	v_ashrrev_i32_e32 v181, 31, v180
	v_lshlrev_b64 v[180:181], 11, v[180:181]
	v_lshl_add_u64 v[180:181], v[180:181], 0, v[146:147]
	v_lshl_add_u64 v[178:179], s[38:39], 0, v[178:179]
	v_lshlrev_b64 v[180:181], 1, v[180:181]
	v_lshl_add_u64 v[182:183], s[36:37], 0, v[180:181]
	s_mov_b64 s[20:21], s[18:19]
	s_mov_b64 s[22:23], s[10:11]
	s_mov_b64 s[18:19], s[10:11]
	s_mov_b64 s[14:15], s[10:11]
	s_mov_b32 s50, s52
	s_mov_b32 s51, s45
	s_waitcnt vmcnt(3)
	v_lshlrev_b32_e32 v184, 16, v170
	v_and_b32_e32 v185, 0xffff0000, v170
	v_lshlrev_b32_e32 v170, 16, v171
	v_and_b32_e32 v171, 0xffff0000, v171
	v_lshlrev_b32_e32 v186, 16, v172
	v_and_b32_e32 v187, 0xffff0000, v172
	v_lshlrev_b32_e32 v172, 16, v173
	v_and_b32_e32 v173, 0xffff0000, v173
	s_waitcnt vmcnt(2)
	v_lshlrev_b32_e32 v188, 16, v174
	v_and_b32_e32 v189, 0xffff0000, v174
	v_lshlrev_b32_e32 v174, 16, v175
	v_and_b32_e32 v175, 0xffff0000, v175
	v_lshlrev_b32_e32 v194, 16, v176
	v_and_b32_e32 v195, 0xffff0000, v176
	v_lshlrev_b32_e32 v176, 16, v177
	v_and_b32_e32 v177, 0xffff0000, v177
	v_pk_fma_f32 v[156:157], v[184:185], s[42:43], v[156:157] op_sel_hi:[1,0,1]
	v_pk_fma_f32 v[158:159], v[170:171], s[42:43], v[158:159] op_sel_hi:[1,0,1]
	v_pk_fma_f32 v[152:153], v[186:187], s[42:43], v[152:153] op_sel_hi:[1,0,1]
	v_pk_fma_f32 v[154:155], v[172:173], s[42:43], v[154:155] op_sel_hi:[1,0,1]
	v_pk_fma_f32 v[170:171], v[188:189], s[42:43], v[148:149] op_sel_hi:[1,0,1]
	v_pk_fma_f32 v[172:173], v[174:175], s[42:43], v[150:151] op_sel_hi:[1,0,1]
	v_pk_fma_f32 v[174:175], v[194:195], s[42:43], v[190:191] op_sel_hi:[1,0,1]
	v_pk_fma_f32 v[176:177], v[176:177], s[42:43], v[192:193] op_sel_hi:[1,0,1]
	v_cvt_pk_bf16_f32 v149, v158, v159
	v_cvt_pk_bf16_f32 v148, v156, v157
	v_cvt_pk_bf16_f32 v151, v154, v155
	v_cvt_pk_bf16_f32 v150, v152, v153
	v_cvt_pk_bf16_f32 v153, v172, v173
	v_cvt_pk_bf16_f32 v152, v170, v171
	v_cvt_pk_bf16_f32 v155, v176, v177
	v_cvt_pk_bf16_f32 v154, v174, v175
	global_store_dwordx4 v[178:179], v[148:151], off sc1
	global_store_dwordx4 v[178:179], v[152:155], off offset:64 sc1
	v_lshl_add_u64 v[198:199], v[198:199], 0, s[100:101]
	global_load_dwordx4 v[200:203], v[198:199], off
	global_load_dwordx4 v[204:207], v[198:199], off offset:64
	s_nop 0
	v_add_u32_e32 v156, 32, v144
	v_ashrrev_i32_e32 v157, 31, v156
	v_lshlrev_b64 v[156:157], 11, v[156:157]
	v_lshl_add_u64 v[156:157], v[156:157], 0, v[146:147]
	v_lshlrev_b64 v[156:157], 1, v[156:157]
	v_lshl_add_u64 v[158:159], s[38:39], 0, v[180:181]
	v_lshl_add_u64 v[170:171], s[36:37], 0, v[156:157]
	s_waitcnt vmcnt(5)
	v_lshlrev_b32_e32 v172, 16, v208
	v_and_b32_e32 v173, 0xffff0000, v208
	v_lshlrev_b32_e32 v148, 16, v209
	v_and_b32_e32 v149, 0xffff0000, v209
	v_lshlrev_b32_e32 v174, 16, v210
	v_and_b32_e32 v175, 0xffff0000, v210
	v_lshlrev_b32_e32 v150, 16, v211
	v_and_b32_e32 v151, 0xffff0000, v211
	s_waitcnt vmcnt(4)
	v_lshlrev_b32_e32 v176, 16, v212
	v_and_b32_e32 v177, 0xffff0000, v212
	v_lshlrev_b32_e32 v152, 16, v213
	v_and_b32_e32 v153, 0xffff0000, v213
	v_lshlrev_b32_e32 v178, 16, v214
	v_and_b32_e32 v179, 0xffff0000, v214
	v_lshlrev_b32_e32 v154, 16, v215
	v_and_b32_e32 v155, 0xffff0000, v215
	v_pk_fma_f32 v[136:137], v[172:173], s[42:43], v[136:137] op_sel_hi:[1,0,1]
	v_pk_fma_f32 v[138:139], v[148:149], s[42:43], v[138:139] op_sel_hi:[1,0,1]
	v_pk_fma_f32 v[148:149], v[174:175], s[42:43], v[128:129] op_sel_hi:[1,0,1]
	v_pk_fma_f32 v[130:131], v[150:151], s[42:43], v[130:131] op_sel_hi:[1,0,1]
	v_pk_fma_f32 v[150:151], v[176:177], s[42:43], v[132:133] op_sel_hi:[1,0,1]
	v_pk_fma_f32 v[132:133], v[152:153], s[42:43], v[134:135] op_sel_hi:[1,0,1]
	v_pk_fma_f32 v[140:141], v[178:179], s[42:43], v[140:141] op_sel_hi:[1,0,1]
	v_pk_fma_f32 v[134:135], v[154:155], s[42:43], v[142:143] op_sel_hi:[1,0,1]
	v_cvt_pk_bf16_f32 v129, v138, v139
	v_cvt_pk_bf16_f32 v128, v136, v137
	v_cvt_pk_bf16_f32 v131, v130, v131
	v_cvt_pk_bf16_f32 v130, v148, v149
	v_cvt_pk_bf16_f32 v133, v132, v133
	v_cvt_pk_bf16_f32 v132, v150, v151
	v_cvt_pk_bf16_f32 v135, v134, v135
	v_cvt_pk_bf16_f32 v134, v140, v141
	global_store_dwordx4 v[158:159], v[128:131], off sc1
	global_store_dwordx4 v[158:159], v[132:135], off offset:64 sc1
	v_lshl_add_u64 v[198:199], v[198:199], 0, s[100:101]
	global_load_dwordx4 v[208:211], v[198:199], off
	global_load_dwordx4 v[212:215], v[198:199], off offset:64
	s_nop 0
	v_add_u32_e32 v136, 48, v144
	v_ashrrev_i32_e32 v137, 31, v136
	v_lshlrev_b64 v[136:137], 11, v[136:137]
	v_lshl_add_u64 v[136:137], v[136:137], 0, v[146:147]
	v_lshlrev_b64 v[136:137], 1, v[136:137]
	v_lshl_add_u64 v[138:139], s[38:39], 0, v[156:157]
	v_lshl_add_u64 v[140:141], s[36:37], 0, v[136:137]
	s_waitcnt vmcnt(5)
	v_lshlrev_b32_e32 v142, 16, v200
	v_and_b32_e32 v143, 0xffff0000, v200
	v_lshlrev_b32_e32 v128, 16, v201
	v_and_b32_e32 v129, 0xffff0000, v201
	v_lshlrev_b32_e32 v148, 16, v202
	v_and_b32_e32 v149, 0xffff0000, v202
	v_lshlrev_b32_e32 v130, 16, v203
	v_and_b32_e32 v131, 0xffff0000, v203
	s_waitcnt vmcnt(4)
	v_lshlrev_b32_e32 v150, 16, v204
	v_and_b32_e32 v151, 0xffff0000, v204
	v_lshlrev_b32_e32 v132, 16, v205
	v_and_b32_e32 v133, 0xffff0000, v205
	v_lshlrev_b32_e32 v152, 16, v206
	v_and_b32_e32 v153, 0xffff0000, v206
	v_lshlrev_b32_e32 v134, 16, v207
	v_and_b32_e32 v135, 0xffff0000, v207
	v_pk_fma_f32 v[124:125], v[142:143], s[42:43], v[124:125] op_sel_hi:[1,0,1]
	v_pk_fma_f32 v[126:127], v[128:129], s[42:43], v[126:127] op_sel_hi:[1,0,1]
	v_pk_fma_f32 v[120:121], v[148:149], s[42:43], v[120:121] op_sel_hi:[1,0,1]
	v_pk_fma_f32 v[122:123], v[130:131], s[42:43], v[122:123] op_sel_hi:[1,0,1]
	v_pk_fma_f32 v[128:129], v[150:151], s[42:43], v[112:113] op_sel_hi:[1,0,1]
	v_pk_fma_f32 v[130:131], v[132:133], s[42:43], v[114:115] op_sel_hi:[1,0,1]
	v_pk_fma_f32 v[132:133], v[152:153], s[42:43], v[116:117] op_sel_hi:[1,0,1]
	v_pk_fma_f32 v[118:119], v[134:135], s[42:43], v[118:119] op_sel_hi:[1,0,1]
	v_cvt_pk_bf16_f32 v113, v126, v127
	v_cvt_pk_bf16_f32 v112, v124, v125
	v_cvt_pk_bf16_f32 v115, v122, v123
	v_cvt_pk_bf16_f32 v114, v120, v121
	v_cvt_pk_bf16_f32 v117, v130, v131
	v_cvt_pk_bf16_f32 v116, v128, v129
	v_cvt_pk_bf16_f32 v119, v118, v119
	v_cvt_pk_bf16_f32 v118, v132, v133
	global_store_dwordx4 v[138:139], v[112:115], off sc1
	global_store_dwordx4 v[138:139], v[116:119], off offset:64 sc1
	v_lshl_add_u64 v[198:199], v[198:199], 0, s[100:101]
	global_load_dwordx4 v[200:203], v[198:199], off
	global_load_dwordx4 v[204:207], v[198:199], off offset:64
	s_nop 0
	v_add_u32_e32 v120, 64, v144
	v_ashrrev_i32_e32 v121, 31, v120
	v_lshlrev_b64 v[120:121], 11, v[120:121]
	v_lshl_add_u64 v[120:121], v[120:121], 0, v[146:147]
	v_lshlrev_b64 v[120:121], 1, v[120:121]
	v_lshl_add_u64 v[122:123], s[38:39], 0, v[136:137]
	v_lshl_add_u64 v[124:125], s[36:37], 0, v[120:121]
	s_waitcnt vmcnt(5)
	v_lshlrev_b32_e32 v126, 16, v208
	v_and_b32_e32 v127, 0xffff0000, v208
	v_lshlrev_b32_e32 v112, 16, v209
	v_and_b32_e32 v113, 0xffff0000, v209
	v_lshlrev_b32_e32 v128, 16, v210
	v_and_b32_e32 v129, 0xffff0000, v210
	v_lshlrev_b32_e32 v114, 16, v211
	v_and_b32_e32 v115, 0xffff0000, v211
	s_waitcnt vmcnt(4)
	v_lshlrev_b32_e32 v130, 16, v212
	v_and_b32_e32 v131, 0xffff0000, v212
	v_lshlrev_b32_e32 v116, 16, v213
	v_and_b32_e32 v117, 0xffff0000, v213
	v_lshlrev_b32_e32 v132, 16, v214
	v_and_b32_e32 v133, 0xffff0000, v214
	v_lshlrev_b32_e32 v118, 16, v215
	v_and_b32_e32 v119, 0xffff0000, v215
	v_pk_fma_f32 v[104:105], v[126:127], s[42:43], v[104:105] op_sel_hi:[1,0,1]
	v_pk_fma_f32 v[106:107], v[112:113], s[42:43], v[106:107] op_sel_hi:[1,0,1]
	v_pk_fma_f32 v[112:113], v[128:129], s[42:43], v[96:97] op_sel_hi:[1,0,1]
	v_pk_fma_f32 v[98:99], v[114:115], s[42:43], v[98:99] op_sel_hi:[1,0,1]
	v_pk_fma_f32 v[114:115], v[130:131], s[42:43], v[100:101] op_sel_hi:[1,0,1]
	v_pk_fma_f32 v[100:101], v[116:117], s[42:43], v[102:103] op_sel_hi:[1,0,1]
	v_pk_fma_f32 v[108:109], v[132:133], s[42:43], v[108:109] op_sel_hi:[1,0,1]
	v_pk_fma_f32 v[102:103], v[118:119], s[42:43], v[110:111] op_sel_hi:[1,0,1]
	v_cvt_pk_bf16_f32 v97, v106, v107
	v_cvt_pk_bf16_f32 v96, v104, v105
	v_cvt_pk_bf16_f32 v99, v98, v99
	v_cvt_pk_bf16_f32 v98, v112, v113
	v_cvt_pk_bf16_f32 v101, v100, v101
	v_cvt_pk_bf16_f32 v100, v114, v115
	v_cvt_pk_bf16_f32 v103, v102, v103
	v_cvt_pk_bf16_f32 v102, v108, v109
	global_store_dwordx4 v[122:123], v[96:99], off sc1
	global_store_dwordx4 v[122:123], v[100:103], off offset:64 sc1
	v_lshl_add_u64 v[198:199], v[198:199], 0, s[100:101]
	global_load_dwordx4 v[208:211], v[198:199], off
	global_load_dwordx4 v[212:215], v[198:199], off offset:64
	s_nop 0
	v_add_u32_e32 v104, 0x50, v144
	v_ashrrev_i32_e32 v105, 31, v104
	v_lshlrev_b64 v[104:105], 11, v[104:105]
	v_lshl_add_u64 v[104:105], v[104:105], 0, v[146:147]
	v_lshlrev_b64 v[104:105], 1, v[104:105]
	v_lshl_add_u64 v[106:107], s[38:39], 0, v[120:121]
	v_lshl_add_u64 v[108:109], s[36:37], 0, v[104:105]
	s_waitcnt vmcnt(5)
	v_lshlrev_b32_e32 v110, 16, v200
	v_and_b32_e32 v111, 0xffff0000, v200
	v_lshlrev_b32_e32 v96, 16, v201
	v_and_b32_e32 v97, 0xffff0000, v201
	v_lshlrev_b32_e32 v112, 16, v202
	v_and_b32_e32 v113, 0xffff0000, v202
	v_lshlrev_b32_e32 v98, 16, v203
	v_and_b32_e32 v99, 0xffff0000, v203
	s_waitcnt vmcnt(4)
	v_lshlrev_b32_e32 v114, 16, v204
	v_and_b32_e32 v115, 0xffff0000, v204
	v_lshlrev_b32_e32 v100, 16, v205
	v_and_b32_e32 v101, 0xffff0000, v205
	v_lshlrev_b32_e32 v116, 16, v206
	v_and_b32_e32 v117, 0xffff0000, v206
	v_lshlrev_b32_e32 v102, 16, v207
	v_and_b32_e32 v103, 0xffff0000, v207
	v_pk_fma_f32 v[92:93], v[110:111], s[42:43], v[92:93] op_sel_hi:[1,0,1]
	v_pk_fma_f32 v[94:95], v[96:97], s[42:43], v[94:95] op_sel_hi:[1,0,1]
	v_pk_fma_f32 v[88:89], v[112:113], s[42:43], v[88:89] op_sel_hi:[1,0,1]
	v_pk_fma_f32 v[90:91], v[98:99], s[42:43], v[90:91] op_sel_hi:[1,0,1]
	v_pk_fma_f32 v[96:97], v[114:115], s[42:43], v[80:81] op_sel_hi:[1,0,1]
	v_pk_fma_f32 v[98:99], v[100:101], s[42:43], v[82:83] op_sel_hi:[1,0,1]
	v_pk_fma_f32 v[100:101], v[116:117], s[42:43], v[84:85] op_sel_hi:[1,0,1]
	v_pk_fma_f32 v[86:87], v[102:103], s[42:43], v[86:87] op_sel_hi:[1,0,1]
	v_cvt_pk_bf16_f32 v81, v94, v95
	v_cvt_pk_bf16_f32 v80, v92, v93
	v_cvt_pk_bf16_f32 v83, v90, v91
	v_cvt_pk_bf16_f32 v82, v88, v89
	v_cvt_pk_bf16_f32 v85, v98, v99
	v_cvt_pk_bf16_f32 v84, v96, v97
	v_cvt_pk_bf16_f32 v87, v86, v87
	v_cvt_pk_bf16_f32 v86, v100, v101
	global_store_dwordx4 v[106:107], v[80:83], off sc1
	global_store_dwordx4 v[106:107], v[84:87], off offset:64 sc1
	v_lshl_add_u64 v[198:199], v[198:199], 0, s[100:101]
	global_load_dwordx4 v[200:203], v[198:199], off
	global_load_dwordx4 v[204:207], v[198:199], off offset:64
	s_nop 0
	v_add_u32_e32 v88, 0x60, v144
	v_ashrrev_i32_e32 v89, 31, v88
	v_lshlrev_b64 v[88:89], 11, v[88:89]
	v_lshl_add_u64 v[88:89], v[88:89], 0, v[146:147]
	v_lshlrev_b64 v[88:89], 1, v[88:89]
	v_lshl_add_u64 v[90:91], s[38:39], 0, v[104:105]
	v_lshl_add_u64 v[92:93], s[36:37], 0, v[88:89]
	s_waitcnt vmcnt(5)
; DI int lane_id() { int l; asm volatile("v_mbcnt_lo_u32_b32 %0, -1, 0\n\tv_mbcnt_hi_u32_b32 %0, -1, %0" : "=v"(l)); return l; }
;     ...
;         { const int l2 = lane_id(); cur.ep(acc, wr, wc, l2 & 15, l2 >> 4); }
;         if (!has_next) break;
	v_lshlrev_b32_e32 v94, 16, v208
	v_and_b32_e32 v95, 0xffff0000, v208
	v_lshlrev_b32_e32 v80, 16, v209
	v_and_b32_e32 v81, 0xffff0000, v209
	v_lshlrev_b32_e32 v96, 16, v210
	v_and_b32_e32 v97, 0xffff0000, v210
	v_lshlrev_b32_e32 v82, 16, v211
	v_and_b32_e32 v83, 0xffff0000, v211
	s_waitcnt vmcnt(4)
	v_lshlrev_b32_e32 v98, 16, v212
	v_and_b32_e32 v99, 0xffff0000, v212
	v_lshlrev_b32_e32 v84, 16, v213
	v_and_b32_e32 v85, 0xffff0000, v213
	v_lshlrev_b32_e32 v100, 16, v214
	v_and_b32_e32 v101, 0xffff0000, v214
	v_lshlrev_b32_e32 v86, 16, v215
	v_and_b32_e32 v87, 0xffff0000, v215
	v_pk_fma_f32 v[72:73], v[94:95], s[42:43], v[72:73] op_sel_hi:[1,0,1]
	v_pk_fma_f32 v[74:75], v[80:81], s[42:43], v[74:75] op_sel_hi:[1,0,1]
	v_pk_fma_f32 v[80:81], v[96:97], s[42:43], v[64:65] op_sel_hi:[1,0,1]
	v_pk_fma_f32 v[66:67], v[82:83], s[42:43], v[66:67] op_sel_hi:[1,0,1]
	v_pk_fma_f32 v[82:83], v[98:99], s[42:43], v[68:69] op_sel_hi:[1,0,1]
	v_pk_fma_f32 v[68:69], v[84:85], s[42:43], v[70:71] op_sel_hi:[1,0,1]
	v_pk_fma_f32 v[76:77], v[100:101], s[42:43], v[76:77] op_sel_hi:[1,0,1]
	v_pk_fma_f32 v[70:71], v[86:87], s[42:43], v[78:79] op_sel_hi:[1,0,1]
	v_cvt_pk_bf16_f32 v65, v74, v75
	v_cvt_pk_bf16_f32 v64, v72, v73
	v_cvt_pk_bf16_f32 v67, v66, v67
	v_cvt_pk_bf16_f32 v66, v80, v81
	v_cvt_pk_bf16_f32 v69, v68, v69
	v_cvt_pk_bf16_f32 v68, v82, v83
	v_cvt_pk_bf16_f32 v71, v70, v71
	v_cvt_pk_bf16_f32 v70, v76, v77
	global_store_dwordx4 v[90:91], v[64:67], off sc1
	global_store_dwordx4 v[90:91], v[68:71], off offset:64 sc1
	v_lshl_add_u64 v[198:199], v[198:199], 0, s[100:101]
	global_load_dwordx4 v[208:211], v[198:199], off
	global_load_dwordx4 v[212:215], v[198:199], off offset:64
	s_nop 0
	v_add_u32_e32 v72, 0x70, v144
	v_ashrrev_i32_e32 v73, 31, v72
	v_lshlrev_b64 v[72:73], 11, v[72:73]
	v_lshl_add_u64 v[72:73], v[72:73], 0, v[146:147]
	v_lshlrev_b64 v[72:73], 1, v[72:73]
	v_lshl_add_u64 v[74:75], s[38:39], 0, v[88:89]
	v_lshl_add_u64 v[76:77], s[36:37], 0, v[72:73]
	s_waitcnt vmcnt(5)
	v_lshlrev_b32_e32 v78, 16, v200
	v_and_b32_e32 v79, 0xffff0000, v200
	v_lshlrev_b32_e32 v64, 16, v201
	v_and_b32_e32 v65, 0xffff0000, v201
	v_lshlrev_b32_e32 v80, 16, v202
	v_and_b32_e32 v81, 0xffff0000, v202
	v_lshlrev_b32_e32 v66, 16, v203
	v_and_b32_e32 v67, 0xffff0000, v203
	s_waitcnt vmcnt(4)
	v_lshlrev_b32_e32 v82, 16, v204
	v_and_b32_e32 v83, 0xffff0000, v204
	v_lshlrev_b32_e32 v68, 16, v205
	v_and_b32_e32 v69, 0xffff0000, v205
	v_lshlrev_b32_e32 v84, 16, v206
	v_and_b32_e32 v85, 0xffff0000, v206
	v_lshlrev_b32_e32 v70, 16, v207
	v_and_b32_e32 v71, 0xffff0000, v207
	v_pk_fma_f32 v[60:61], v[78:79], s[42:43], v[60:61] op_sel_hi:[1,0,1]
	v_pk_fma_f32 v[62:63], v[64:65], s[42:43], v[62:63] op_sel_hi:[1,0,1]
	v_pk_fma_f32 v[56:57], v[80:81], s[42:43], v[56:57] op_sel_hi:[1,0,1]
	v_pk_fma_f32 v[58:59], v[66:67], s[42:43], v[58:59] op_sel_hi:[1,0,1]
	v_pk_fma_f32 v[64:65], v[82:83], s[42:43], v[52:53] op_sel_hi:[1,0,1]
	v_pk_fma_f32 v[52:53], v[68:69], s[42:43], v[54:55] op_sel_hi:[1,0,1]
	v_pk_fma_f32 v[66:67], v[84:85], s[42:43], v[48:49] op_sel_hi:[1,0,1]
	v_pk_fma_f32 v[54:55], v[70:71], s[42:43], v[50:51] op_sel_hi:[1,0,1]
	v_cvt_pk_bf16_f32 v49, v62, v63
	v_cvt_pk_bf16_f32 v48, v60, v61
	v_cvt_pk_bf16_f32 v51, v58, v59
	v_cvt_pk_bf16_f32 v50, v56, v57
	v_cvt_pk_bf16_f32 v53, v52, v53
	v_cvt_pk_bf16_f32 v52, v64, v65
	v_cvt_pk_bf16_f32 v55, v54, v55
	v_cvt_pk_bf16_f32 v54, v66, v67
	global_store_dwordx4 v[74:75], v[48:51], off sc1
	global_store_dwordx4 v[74:75], v[52:55], off offset:64 sc1
	s_nop 0
	v_lshl_add_u64 v[56:57], s[38:39], 0, v[72:73]
	s_waitcnt vmcnt(3)
	v_lshlrev_b32_e32 v58, 16, v208
	v_and_b32_e32 v59, 0xffff0000, v208
	v_lshlrev_b32_e32 v48, 16, v209
	v_and_b32_e32 v49, 0xffff0000, v209
	v_lshlrev_b32_e32 v60, 16, v210
	v_and_b32_e32 v61, 0xffff0000, v210
	v_lshlrev_b32_e32 v50, 16, v211
	v_and_b32_e32 v51, 0xffff0000, v211
	s_waitcnt vmcnt(2)
	v_lshlrev_b32_e32 v62, 16, v212
	v_and_b32_e32 v63, 0xffff0000, v212
	v_lshlrev_b32_e32 v52, 16, v213
	v_and_b32_e32 v53, 0xffff0000, v213
	v_lshlrev_b32_e32 v64, 16, v214
	v_and_b32_e32 v65, 0xffff0000, v214
	v_lshlrev_b32_e32 v54, 16, v215
	v_and_b32_e32 v55, 0xffff0000, v215
	v_pk_fma_f32 v[40:41], v[58:59], s[42:43], v[40:41] op_sel_hi:[1,0,1]
	v_pk_fma_f32 v[42:43], v[48:49], s[42:43], v[42:43] op_sel_hi:[1,0,1]
	v_pk_fma_f32 v[36:37], v[60:61], s[42:43], v[36:37] op_sel_hi:[1,0,1]
	v_pk_fma_f32 v[38:39], v[50:51], s[42:43], v[38:39] op_sel_hi:[1,0,1]
	v_pk_fma_f32 v[48:49], v[62:63], s[42:43], v[32:33] op_sel_hi:[1,0,1]
	v_pk_fma_f32 v[50:51], v[52:53], s[42:43], v[34:35] op_sel_hi:[1,0,1]
	v_pk_fma_f32 v[44:45], v[64:65], s[42:43], v[44:45] op_sel_hi:[1,0,1]
	v_pk_fma_f32 v[46:47], v[54:55], s[42:43], v[46:47] op_sel_hi:[1,0,1]
	v_cvt_pk_bf16_f32 v33, v42, v43
	v_cvt_pk_bf16_f32 v32, v40, v41
	v_cvt_pk_bf16_f32 v35, v38, v39
	v_cvt_pk_bf16_f32 v34, v36, v37
	v_cvt_pk_bf16_f32 v37, v50, v51
	v_cvt_pk_bf16_f32 v36, v48, v49
	v_cvt_pk_bf16_f32 v39, v46, v47
	v_cvt_pk_bf16_f32 v38, v44, v45
	global_store_dwordx4 v[56:57], v[32:35], off sc1
	global_store_dwordx4 v[56:57], v[36:39], off offset:64 sc1
	s_cbranch_vccnz .LBB0_382

; DI float bflo(unsigned w) { return __uint_as_float(w << 16); }
; DI float bfhi(unsigned w) { return __uint_as_float(w & 0xffff0000u); }
; DI u32x2 pack4(f32x4 v) { bf16x4_t r = __builtin_convertvector(v, bf16x4_t); return __builtin_bit_cast(u32x2, r); }
; DI void p4_ln_router(const Ctx& c) {
;     ...
;             const float rstd = rsqrtf(qv * (1.0f / D) + LN_EPS);
;             if (lane == 0) { st1[2 * tok] = mean; st1[2 * tok + 1] = rstd; }
; #pragma unroll
;             for (int i = 0; i < 8; ++i) { const int d = (i * 64 + lane) * 4; const f32x4 g = *(const f32x4*)(lw + d), bb = *(const f32x4*)(lb + d);
;                 const f32x4 xv = (v[i] - mean) * rstd * g + bb;
;                 const u32x2 hi = pack4(xv); const f32x4 rsd = {xv[0] - bflo(hi.x), xv[1] - bfhi(hi.x), xv[2] - bflo(hi.y), xv[3] - bfhi(hi.y)};
;                 *(u32x2*)(x1b + (size_t)tok * D + d) = hi;
;                 *LP(u32x2, Xhi + tl * XSTR + d * 2) = hi; *LP(u32x2, Xlo + tl * XSTR + d * 2) = pack4(rsd); } }
.LBB0_442:
	s_or_b64 exec, exec, s[26:27]
	v_mov_b32_e32 v68, v62
	v_mov_b32_e32 v69, v60
	v_mov_b32_e32 v72, v66
	v_mov_b32_e32 v73, v64
	v_pk_mul_f32 v[72:73], v[72:73], v[4:5] op_sel_hi:[1,0]
	v_pk_mul_f32 v[120:121], v[68:69], v[4:5] op_sel_hi:[1,0]
	s_lshl_b64 s[24:25], s[24:25], 11
	v_lshl_add_u64 v[68:69], s[24:25], 1, v[52:53]
	v_mov_b32_e32 v60, v63
	v_mov_b32_e32 v64, v67
	v_pk_mul_f32 v[62:63], v[64:65], v[4:5] op_sel_hi:[1,0]
	v_pk_mul_f32 v[64:65], v[60:61], v[4:5] op_sel_hi:[1,0]
	v_mov_b32_e32 v57, v58
	v_pk_mul_f32 v[58:59], v[78:79], v[4:5] op_sel_hi:[1,0]
	v_pk_mul_f32 v[56:57], v[56:57], v[4:5] op_sel_hi:[1,0]
	v_pk_mul_f32 v[54:55], v[54:55], v[4:5] op_sel_hi:[1,0]
	v_pk_mul_f32 v[22:23], v[22:23], v[4:5] op_sel_hi:[1,0]
	v_mov_b32_e32 v14, v19
	v_mov_b32_e32 v16, v21
	v_pk_mul_f32 v[16:17], v[16:17], v[4:5] op_sel_hi:[1,0]
	v_pk_mul_f32 v[14:15], v[14:15], v[4:5] op_sel_hi:[1,0]
	v_mov_b32_e32 v11, v12
	v_pk_mul_f32 v[12:13], v[70:71], v[4:5] op_sel_hi:[1,0]
	v_pk_mul_f32 v[10:11], v[10:11], v[4:5] op_sel_hi:[1,0]
	v_pk_mul_f32 v[8:9], v[8:9], v[4:5] op_sel_hi:[1,0]
	v_pk_mul_f32 v[6:7], v[6:7], v[4:5] op_sel_hi:[1,0]
	v_mov_b32_e32 v0, v5
	v_pk_mul_f32 v[124:125], v[0:1], v[4:5] op_sel_hi:[1,0]
	s_mul_i32 s25, s36, 0x1010
	s_xor_b64 s[26:27], s[22:23], -1
	s_add_i32 s25, s25, 0
	s_and_b64 vcc, exec, s[26:27]
	s_add_i32 s26, s25, 0x10100
	v_add_u32_e32 v115, s25, v89
	v_add_u32_e32 v133, s26, v89
	v_add_u32_e32 v126, s25, v90
	v_add_u32_e32 v134, s26, v90
	v_add_u32_e32 v127, s25, v91
	v_add_u32_e32 v135, s26, v91
	v_add_u32_e32 v128, s25, v92
	v_add_u32_e32 v136, s26, v92
	v_add_u32_e32 v129, s25, v93
	v_add_u32_e32 v137, s26, v93
	v_add_u32_e32 v130, s25, v94
	v_add_u32_e32 v138, s26, v94
	v_add_u32_e32 v131, s25, v95
	v_add_u32_e32 v139, s26, v95
	s_mov_b32 s24, 1
	s_mov_b64 s[22:23], 0
	v_add_u32_e32 v132, s25, v96
	v_add_u32_e32 v140, s26, v96
	s_waitcnt vmcnt(0)
	v_pk_fma_f32 v[72:73], v[72:73], v[174:175], v[178:179]
	v_pk_fma_f32 v[74:75], v[120:121], v[172:173], v[176:177]
	v_cvt_pk_bf16_f32 v77, v72, v73
	v_cvt_pk_bf16_f32 v76, v74, v75
	global_store_dwordx2 v[68:69], v[76:77], off sc1
	v_pk_fma_f32 v[60:61], v[62:63], v[182:183], v[186:187]
	v_pk_fma_f32 v[62:63], v[64:65], v[180:181], v[184:185]
	v_cvt_pk_bf16_f32 v65, v60, v61
	v_cvt_pk_bf16_f32 v64, v62, v63
	global_store_dwordx2 v[68:69], v[64:65], off offset:512 sc1
	v_pk_fma_f32 v[66:67], v[58:59], v[190:191], v[194:195]
	v_pk_fma_f32 v[78:79], v[56:57], v[188:189], v[192:193]
	v_cvt_pk_bf16_f32 v121, v66, v67
	v_cvt_pk_bf16_f32 v120, v78, v79
	global_store_dwordx2 v[68:69], v[120:121], off offset:1024 sc1
	v_pk_fma_f32 v[58:59], v[54:55], v[202:203], v[206:207]
	v_pk_fma_f32 v[22:23], v[22:23], v[200:201], v[204:205]
	v_cvt_pk_bf16_f32 v123, v58, v59
	v_cvt_pk_bf16_f32 v122, v22, v23
	global_store_dwordx2 v[68:69], v[122:123], off offset:1536 sc1
	v_pk_fma_f32 v[56:57], v[16:17], v[210:211], v[214:215]
	v_pk_fma_f32 v[54:55], v[14:15], v[208:209], v[212:213]
	v_cvt_pk_bf16_f32 v117, v56, v57
	v_cvt_pk_bf16_f32 v116, v54, v55
	global_store_dwordx2 v[68:69], v[116:117], off offset:2048 sc1
	v_pk_mul_f32 v[118:119], v[2:3], v[4:5] op_sel_hi:[1,0]
	v_pk_fma_f32 v[20:21], v[12:13], v[218:219], v[222:223]
	v_pk_fma_f32 v[18:19], v[10:11], v[216:217], v[220:221]
	v_cvt_pk_bf16_f32 v71, v20, v21
	v_cvt_pk_bf16_f32 v70, v18, v19
	global_store_dwordx2 v[68:69], v[70:71], off offset:2560 sc1
	v_pk_fma_f32 v[8:9], v[8:9], v[226:227], v[230:231]
	v_pk_fma_f32 v[10:11], v[6:7], v[224:225], v[228:229]
	v_cvt_pk_bf16_f32 v13, v8, v9
	v_cvt_pk_bf16_f32 v12, v10, v11
	global_store_dwordx2 v[68:69], v[12:13], off offset:3072 sc1
	v_lshlrev_b32_e32 v14, 16, v76
	v_and_b32_e32 v15, 0xffff0000, v76
	v_lshlrev_b32_e32 v16, 16, v77
	v_and_b32_e32 v17, 0xffff0000, v77
	v_pk_add_f32 v[14:15], v[74:75], v[14:15] neg_lo:[0,1] neg_hi:[0,1]
	v_pk_add_f32 v[16:17], v[72:73], v[16:17] neg_lo:[0,1] neg_hi:[0,1]
	ds_write_b64 v115, v[76:77]
	v_cvt_pk_bf16_f32 v17, v16, v17
	v_cvt_pk_bf16_f32 v16, v14, v15
	ds_write_b64 v133, v[16:17]
	v_lshlrev_b32_e32 v14, 16, v64
	v_and_b32_e32 v15, 0xffff0000, v64
	v_lshlrev_b32_e32 v16, 16, v65
	v_and_b32_e32 v17, 0xffff0000, v65
	v_pk_add_f32 v[14:15], v[62:63], v[14:15] neg_lo:[0,1] neg_hi:[0,1]
	v_pk_add_f32 v[16:17], v[60:61], v[16:17] neg_lo:[0,1] neg_hi:[0,1]
	ds_write_b64 v126, v[64:65]
	v_cvt_pk_bf16_f32 v17, v16, v17
	v_cvt_pk_bf16_f32 v16, v14, v15
	ds_write_b64 v134, v[16:17]
	v_lshlrev_b32_e32 v14, 16, v120
	v_and_b32_e32 v15, 0xffff0000, v120
	v_lshlrev_b32_e32 v16, 16, v121
	v_and_b32_e32 v17, 0xffff0000, v121
	v_pk_add_f32 v[14:15], v[78:79], v[14:15] neg_lo:[0,1] neg_hi:[0,1]
	v_pk_add_f32 v[16:17], v[66:67], v[16:17] neg_lo:[0,1] neg_hi:[0,1]
	ds_write_b64 v127, v[120:121]
	v_cvt_pk_bf16_f32 v17, v16, v17
	v_cvt_pk_bf16_f32 v16, v14, v15
	ds_write_b64 v135, v[16:17]
	v_lshlrev_b32_e32 v14, 16, v122
	v_and_b32_e32 v15, 0xffff0000, v122
	v_lshlrev_b32_e32 v16, 16, v123
	v_and_b32_e32 v17, 0xffff0000, v123
	v_pk_add_f32 v[14:15], v[22:23], v[14:15] neg_lo:[0,1] neg_hi:[0,1]
	v_pk_add_f32 v[16:17], v[58:59], v[16:17] neg_lo:[0,1] neg_hi:[0,1]
	ds_write_b64 v128, v[122:123]
	v_cvt_pk_bf16_f32 v17, v16, v17
	v_cvt_pk_bf16_f32 v16, v14, v15
	ds_write_b64 v136, v[16:17]
	v_lshlrev_b32_e32 v14, 16, v116
	v_and_b32_e32 v15, 0xffff0000, v116
	v_lshlrev_b32_e32 v16, 16, v117
	v_and_b32_e32 v17, 0xffff0000, v117
	v_pk_add_f32 v[14:15], v[54:55], v[14:15] neg_lo:[0,1] neg_hi:[0,1]
	v_pk_add_f32 v[16:17], v[56:57], v[16:17] neg_lo:[0,1] neg_hi:[0,1]
	ds_write_b64 v129, v[116:117]
	v_cvt_pk_bf16_f32 v17, v16, v17
	v_cvt_pk_bf16_f32 v16, v14, v15
; DI float bflo(unsigned w) { return __uint_as_float(w << 16); }
; DI float bfhi(unsigned w) { return __uint_as_float(w & 0xffff0000u); }
; DI u32x2 pack4(f32x4 v) { bf16x4_t r = __builtin_convertvector(v, bf16x4_t); return __builtin_bit_cast(u32x2, r); }
; DI void p4_ln_router(const Ctx& c) {
;     ...
;         for (int tt = 0; tt < 2; ++tt) { const int tl = 2 * w + tt, tok = tokbase + pass * 16 + tl;
;             const u32x2* src = (const u32x2*)(y1 + (size_t)tok * D); f32x4 v[8]; float s = 0.f;
; #pragma unroll
;             for (int i = 0; i < 8; ++i) { const u32x2 yv = src[i * 64 + lane]; v[i] = (f32x4){bflo(yv.x), bfhi(yv.x), bflo(yv.y), bfhi(yv.y)}; s += (v[i][0] + v[i][1]) + (v[i][2] + v[i][3]); }
; #pragma unroll
;             for (int o = 32; o >= 1; o >>= 1) s += __shfl_xor(s, o);
;     ...
;             for (int i = 0; i < 8; ++i) { const int d = (i * 64 + lane) * 4; const f32x4 g = *(const f32x4*)(lw + d), bb = *(const f32x4*)(lb + d);
;                 const f32x4 xv = (v[i] - mean) * rstd * g + bb;
;                 const u32x2 hi = pack4(xv); const f32x4 rsd = {xv[0] - bflo(hi.x), xv[1] - bfhi(hi.x), xv[2] - bflo(hi.y), xv[3] - bfhi(hi.y)};
;                 *(u32x2*)(x1b + (size_t)tok * D + d) = hi;
;                 *LP(u32x2, Xhi + tl * XSTR + d * 2) = hi; *LP(u32x2, Xlo + tl * XSTR + d * 2) = pack4(rsd); } }
	ds_write_b64 v137, v[16:17]
	v_lshlrev_b32_e32 v14, 16, v70
	v_and_b32_e32 v15, 0xffff0000, v70
	v_lshlrev_b32_e32 v16, 16, v71
	v_and_b32_e32 v17, 0xffff0000, v71
	v_pk_add_f32 v[14:15], v[18:19], v[14:15] neg_lo:[0,1] neg_hi:[0,1]
	v_pk_add_f32 v[16:17], v[20:21], v[16:17] neg_lo:[0,1] neg_hi:[0,1]
	ds_write_b64 v130, v[70:71]
	v_cvt_pk_bf16_f32 v17, v16, v17
	v_cvt_pk_bf16_f32 v16, v14, v15
	ds_write_b64 v138, v[16:17]
	v_lshlrev_b32_e32 v14, 16, v12
	v_and_b32_e32 v15, 0xffff0000, v12
	v_lshlrev_b32_e32 v16, 16, v13
	v_and_b32_e32 v17, 0xffff0000, v13
	v_pk_add_f32 v[10:11], v[10:11], v[14:15] neg_lo:[0,1] neg_hi:[0,1]
	v_pk_add_f32 v[8:9], v[8:9], v[16:17] neg_lo:[0,1] neg_hi:[0,1]
	ds_write_b64 v131, v[12:13]
	v_cvt_pk_bf16_f32 v9, v8, v9
	v_cvt_pk_bf16_f32 v8, v10, v11
	ds_write_b64 v139, v[8:9]
	v_pk_fma_f32 v[2:3], v[124:125], v[234:235], v[238:239]
	v_pk_fma_f32 v[0:1], v[118:119], v[232:233], v[236:237]
	v_cvt_pk_bf16_f32 v5, v2, v3
	v_cvt_pk_bf16_f32 v4, v0, v1
	v_lshlrev_b32_e32 v6, 16, v4
	v_and_b32_e32 v7, 0xffff0000, v4
	v_lshlrev_b32_e32 v8, 16, v5
	v_and_b32_e32 v9, 0xffff0000, v5
	v_pk_add_f32 v[0:1], v[0:1], v[6:7] neg_lo:[0,1] neg_hi:[0,1]
	v_pk_add_f32 v[2:3], v[2:3], v[8:9] neg_lo:[0,1] neg_hi:[0,1]
	global_store_dwordx2 v[68:69], v[4:5], off offset:3584 sc1
	v_cvt_pk_bf16_f32 v3, v2, v3
	v_cvt_pk_bf16_f32 v2, v0, v1
	ds_write_b64 v132, v[4:5]
	ds_write_b64 v140, v[2:3]
	s_cbranch_vccnz .LBB0_445
.LBB0_443:
	s_or_b32 s36, s24, s5
	s_add_i32 s24, s31, s36
	s_ashr_i32 s25, s24, 31
	s_lshl_b64 s[26:27], s[24:25], 12
	v_lshl_add_u64 v[0:1], v[50:51], 0, s[26:27]
	global_load_dwordx2 v[2:3], v[0:1], off offset:512
	global_load_dwordx2 v[4:5], v[0:1], off
	global_load_dwordx2 v[6:7], v[0:1], off offset:1024
	global_load_dwordx2 v[8:9], v[0:1], off offset:1536
	global_load_dwordx2 v[10:11], v[0:1], off offset:2048
	global_load_dwordx2 v[12:13], v[0:1], off offset:2560
	global_load_dwordx2 v[68:69], v[0:1], off offset:3072
	global_load_dwordx2 v[70:71], v[0:1], off offset:3584
	s_waitcnt vmcnt(7)
	v_lshlrev_b32_e32 v63, 16, v2
	s_waitcnt vmcnt(6)
	v_lshlrev_b32_e32 v62, 16, v4
	v_and_b32_e32 v61, 0xffff0000, v2
	v_and_b32_e32 v60, 0xffff0000, v4
	v_lshlrev_b32_e32 v67, 16, v3
	v_lshlrev_b32_e32 v66, 16, v5
	v_and_b32_e32 v65, 0xffff0000, v3
	v_and_b32_e32 v64, 0xffff0000, v5
	s_waitcnt vmcnt(5)
	v_lshlrev_b32_e32 v57, 16, v7
	v_lshlrev_b32_e32 v56, 16, v6
	v_and_b32_e32 v59, 0xffff0000, v7
	v_and_b32_e32 v58, 0xffff0000, v6
	s_waitcnt vmcnt(4)
	v_lshlrev_b32_e32 v22, 16, v8
	v_and_b32_e32 v23, 0xffff0000, v8
	v_lshlrev_b32_e32 v54, 16, v9
	v_and_b32_e32 v55, 0xffff0000, v9
	s_waitcnt vmcnt(1)
	v_lshlrev_b32_e32 v6, 16, v68
	v_and_b32_e32 v7, 0xffff0000, v68
	v_lshlrev_b32_e32 v8, 16, v69
	v_and_b32_e32 v9, 0xffff0000, v69
	s_waitcnt vmcnt(0)
	v_lshlrev_b32_e32 v2, 16, v70
	v_and_b32_e32 v3, 0xffff0000, v70
	v_lshlrev_b32_e32 v5, 16, v71
	v_and_b32_e32 v1, 0xffff0000, v71
	v_pk_add_f32 v[68:69], v[62:63], v[60:61]
	v_pk_add_f32 v[70:71], v[66:67], v[64:65]
	v_pk_add_f32 v[72:73], v[56:57], v[58:59]
	v_add_f32_e32 v4, v6, v7
	v_add_f32_e32 v0, v8, v9
	v_pk_add_f32 v[68:69], v[68:69], v[70:71]
	v_and_b32_e32 v15, 0xffff0000, v10
	v_pk_add_f32 v[70:71], v[72:73], v[72:73] op_sel:[0,1] op_sel_hi:[1,0]
	v_pk_add_f32 v[76:77], v[4:5], v[0:1]
	v_add_f32_e32 v0, 0, v68
	v_lshlrev_b32_e32 v19, 16, v10
	v_lshlrev_b32_e32 v21, 16, v11
	v_and_b32_e32 v17, 0xffff0000, v11
	v_add_f32_e32 v20, v22, v23
	v_add_f32_e32 v16, v54, v55
	v_mov_b32_e32 v71, v15
	v_add_f32_e32 v18, v0, v69
	v_lshlrev_b32_e32 v11, 16, v13
	v_lshlrev_b32_e32 v10, 16, v12
	v_and_b32_e32 v13, 0xffff0000, v13
	v_and_b32_e32 v12, 0xffff0000, v12
	v_pk_add_f32 v[72:73], v[20:21], v[16:17]
	v_pk_add_f32 v[68:69], v[18:19], v[70:71]
	v_pk_add_f32 v[74:75], v[10:11], v[12:13]
	v_pk_add_f32 v[68:69], v[68:69], v[72:73]
	v_pk_add_f32 v[74:75], v[74:75], v[74:75] op_sel:[0,1] op_sel_hi:[1,0]
	v_pk_add_f32 v[68:69], v[68:69], v[68:69] op_sel:[0,1] op_sel_hi:[1,0]
	v_mov_b32_e32 v75, v3
	v_mov_b32_e32 v69, v2
	v_pk_add_f32 v[68:69], v[68:69], v[74:75]
	s_nop 0
	v_pk_add_f32 v[68:69], v[68:69], v[76:77]
	s_nop 0
	v_add_f32_e32 v0, v68, v69
	ds_bpermute_b32 v4, v83, v0
	s_waitcnt lgkmcnt(0)
	v_add_f32_e32 v0, v0, v4
	ds_bpermute_b32 v4, v84, v0
	s_waitcnt lgkmcnt(0)
	v_add_f32_e32 v0, v0, v4
	ds_bpermute_b32 v4, v85, v0
	s_waitcnt lgkmcnt(0)
; DI void p4_ln_router(const Ctx& c) {
;     ...
;             for (int o = 32; o >= 1; o >>= 1) s += __shfl_xor(s, o);
;             const float mean = s * (1.0f / D); float qv = 0.f;
; #pragma unroll
;             for (int i = 0; i < 8; ++i) { const f32x4 dl = v[i] - mean; qv += (dl[0] * dl[0] + dl[1] * dl[1]) + (dl[2] * dl[2] + dl[3] * dl[3]); }
; #pragma unroll
;             for (int o = 32; o >= 1; o >>= 1) qv += __shfl_xor(qv, o);
;             const float rstd = rsqrtf(qv * (1.0f / D) + LN_EPS);
;             if (lane == 0) { st1[2 * tok] = mean; st1[2 * tok + 1] = rstd; }
	v_add_f32_e32 v0, v0, v4
	ds_bpermute_b32 v4, v86, v0
	s_waitcnt lgkmcnt(0)
	v_add_f32_e32 v0, v0, v4
	ds_bpermute_b32 v4, v87, v0
	s_waitcnt lgkmcnt(0)
	v_add_f32_e32 v0, v0, v4
	ds_bpermute_b32 v4, v88, v0
	s_waitcnt lgkmcnt(0)
	v_add_f32_e32 v0, v0, v4
	v_fmac_f32_e32 v64, 0xba000000, v0
	v_fmac_f32_e32 v60, 0xba000000, v0
	v_fmac_f32_e32 v65, 0xba000000, v0
	v_fmac_f32_e32 v61, 0xba000000, v0
	v_fmac_f32_e32 v59, 0xba000000, v0
	v_fmac_f32_e32 v57, 0xba000000, v0
	v_fmac_f32_e32 v58, 0xba000000, v0
	v_fmac_f32_e32 v66, 0xba000000, v0
	v_fmac_f32_e32 v62, 0xba000000, v0
	v_fmac_f32_e32 v67, 0xba000000, v0
	v_fmac_f32_e32 v63, 0xba000000, v0
	v_fmac_f32_e32 v56, 0xba000000, v0
	v_pk_mul_f32 v[68:69], v[60:61], v[60:61]
	v_pk_mul_f32 v[72:73], v[64:65], v[64:65]
	v_mov_b32_e32 v78, v57
	v_mov_b32_e32 v79, v59
	v_mov_b32_e32 v57, v58
	v_pk_fma_f32 v[68:69], v[62:63], v[62:63], v[68:69]
	v_pk_fma_f32 v[72:73], v[66:67], v[66:67], v[72:73]
	v_pk_mul_f32 v[74:75], v[78:79], v[78:79]
	v_pk_mul_f32 v[76:77], v[56:57], v[56:57]
	v_fmac_f32_e32 v54, 0xba000000, v0
	v_fmac_f32_e32 v22, 0xba000000, v0
	v_pk_add_f32 v[68:69], v[68:69], v[72:73]
	v_pk_mov_b32 v[72:73], v[76:77], v[74:75] op_sel:[1,0]
	v_mov_b32_e32 v77, v75
	v_fmac_f32_e32 v55, 0xba000000, v0
	v_fmac_f32_e32 v23, 0xba000000, v0
	v_fmac_f32_e32 v15, 0xba000000, v0
	v_fmac_f32_e32 v13, 0xba000000, v0
	v_fmac_f32_e32 v11, 0xba000000, v0
	v_fmac_f32_e32 v12, 0xba000000, v0
	v_mul_f32_e32 v4, v22, v22
	v_mul_f32_e32 v14, v54, v54
	v_pk_add_f32 v[72:73], v[72:73], v[76:77]
	v_fmac_f32_e32 v17, 0xba000000, v0
	v_fmac_f32_e32 v21, 0xba000000, v0
	v_fmac_f32_e32 v19, 0xba000000, v0
	v_fmac_f32_e32 v10, 0xba000000, v0
	v_mov_b32_e32 v70, v11
	v_mov_b32_e32 v71, v13
	v_mov_b32_e32 v11, v12
	v_pk_fma_f32 v[116:117], v[22:23], v[22:23], v[4:5] op_sel_hi:[1,1,0]
	v_pk_fma_f32 v[118:119], v[54:55], v[54:55], v[14:15] op_sel_hi:[1,1,0]
	v_pk_add_f32 v[68:69], v[68:69], v[68:69] op_sel_hi:[0,1]
	v_pk_add_f32 v[72:73], v[72:73], v[72:73] op_sel_hi:[0,1]
	v_pk_mul_f32 v[120:121], v[70:71], v[70:71]
	v_pk_mul_f32 v[122:123], v[10:11], v[10:11]
	v_mul_f32_e32 v116, v19, v19
	v_mul_f32_e32 v118, v15, v15
	v_mul_f32_e32 v68, v17, v17
	v_mul_f32_e32 v72, v21, v21
	v_fmac_f32_e32 v6, 0xba000000, v0
	v_fmac_f32_e32 v8, 0xba000000, v0
	v_pk_mov_b32 v[74:75], v[122:123], v[120:121] op_sel:[1,0]
	v_mov_b32_e32 v123, v121
	v_pk_add_f32 v[76:77], v[116:117], v[118:119]
	v_pk_add_f32 v[68:69], v[72:73], v[68:69]
	v_fmac_f32_e32 v7, 0xba000000, v0
	v_mul_f32_e32 v4, v6, v6
	v_fmac_f32_e32 v9, 0xba000000, v0
	v_pk_add_f32 v[74:75], v[74:75], v[122:123]
	v_pk_add_f32 v[68:69], v[76:77], v[68:69]
	v_pk_fma_f32 v[72:73], v[6:7], v[6:7], v[4:5] op_sel_hi:[1,1,0]
	v_mul_f32_e32 v4, v8, v8
	v_pk_add_f32 v[74:75], v[74:75], v[74:75] op_sel_hi:[0,1]
	v_pk_add_f32 v[68:69], v[68:69], v[68:69] op_sel_hi:[0,1]
	v_pk_fma_f32 v[76:77], v[8:9], v[8:9], v[4:5] op_sel_hi:[1,1,0]
	v_fmac_f32_e32 v1, 0xba000000, v0
	v_fmac_f32_e32 v5, 0xba000000, v0
	v_fmac_f32_e32 v3, 0xba000000, v0
	v_fmac_f32_e32 v2, 0xba000000, v0
	v_mul_f32_e32 v72, v2, v2
	v_mul_f32_e32 v76, v3, v3
	v_mul_f32_e32 v74, v5, v5
	v_mul_f32_e32 v68, v1, v1
	v_pk_add_f32 v[72:73], v[72:73], v[76:77]
	v_pk_add_f32 v[68:69], v[74:75], v[68:69]
	s_nop 0
	v_pk_add_f32 v[68:69], v[72:73], v[68:69]
	s_nop 0
	v_add_f32_e32 v4, v68, v69
	ds_bpermute_b32 v11, v83, v4
	s_waitcnt lgkmcnt(0)
	v_add_f32_e32 v4, v4, v11
	ds_bpermute_b32 v11, v84, v4
	s_waitcnt lgkmcnt(0)
	v_add_f32_e32 v4, v4, v11
	ds_bpermute_b32 v11, v85, v4
	s_waitcnt lgkmcnt(0)
	v_add_f32_e32 v4, v4, v11
	ds_bpermute_b32 v11, v86, v4
	s_waitcnt lgkmcnt(0)
	v_add_f32_e32 v4, v4, v11
	ds_bpermute_b32 v11, v87, v4
	s_waitcnt lgkmcnt(0)
	v_add_f32_e32 v4, v4, v11
	ds_bpermute_b32 v11, v88, v4
	s_waitcnt lgkmcnt(0)
	v_add_f32_e32 v4, v4, v11
	v_fmamk_f32 v4, v4, 0x3a000000, v110
	v_mul_f32_e32 v11, 0x4b800000, v4
	v_cmp_gt_f32_e32 vcc, s6, v4
	s_nop 1
	v_cndmask_b32_e32 v4, v4, v11, vcc
	v_rsq_f32_e32 v4, v4
	s_nop 0
	v_mul_f32_e32 v11, 0x45800000, v4
	v_cndmask_b32_e32 v4, v4, v11, vcc
	s_and_saveexec_b64 s[26:27], s[10:11]
	s_cbranch_execz .LBB0_442
	s_lshl_b32 s38, s24, 1
	s_ashr_i32 s39, s38, 31
	s_lshl_b64 s[38:39], s[38:39], 2
	s_add_u32 s38, s3, s38
	v_mul_f32_e32 v68, 0x3a000000, v0
	s_addc_u32 s39, s71, s39
	v_mov_b32_e32 v69, v4
	global_store_dwordx2 v25, v[68:69], s[38:39] sc1
	s_branch .LBB0_442

; DI float bflo(unsigned w) { return __uint_as_float(w << 16); }
; DI float bfhi(unsigned w) { return __uint_as_float(w & 0xffff0000u); }
; DI void p7_ln2(const Ctx& c) {
;     ...
;     for (int tt = 0; tt < 4; ++tt) { const int tok = tb * 32 + c.wid * 4 + tt;
;         const float mean1 = st1[2 * tok], rstd1 = st1[2 * tok + 1];
;         f32x4 z[8]; float s = 0.f;
; #pragma unroll
;         for (int i = 0; i < 4; ++i) { const int d = (i * 64 + lane) * 8; const u32x4 yr = *(const u32x4*)(y1 + (size_t)tok * D + d);
;             const f32x4 y0 = {bflo(yr.x), bfhi(yr.x), bflo(yr.y), bfhi(yr.y)}, y1v = {bflo(yr.z), bfhi(yr.z), bflo(yr.w), bfhi(yr.w)};
;             const f32x4 g0 = *(const f32x4*)(l1w + d), g1 = *(const f32x4*)(l1w + d + 4), b0 = *(const f32x4*)(l1b + d), b1 = *(const f32x4*)(l1b + d + 4);
;             f32x4 a0 = ((y0 - mean1) * rstd1 * g0 + b0) * DN_ALPHA, a1 = ((y1v - mean1) * rstd1 * g1 + b1) * DN_ALPHA;
; #pragma unroll
;             for (int k = 0; k < 4; ++k) { const u32x4 v = *(const u32x4*)(yb + ((size_t)tok * 4 + k) * D + d);
;                 a0[0] += bflo(v.x); a0[1] += bfhi(v.x); a0[2] += bflo(v.y); a0[3] += bfhi(v.y); a1[0] += bflo(v.z); a1[1] += bfhi(v.z); a1[2] += bflo(v.w); a1[3] += bfhi(v.w); }
;             z[2 * i] = a0; z[2 * i + 1] = a1; s += ((a0[0] + a0[1]) + (a0[2] + a0[3])) + ((a1[0] + a1[1]) + (a1[2] + a1[3])); }
.LBB0_977:
	v_lshl_add_u64 v[72:73], s[34:35], 0, v[70:71]
	v_add_co_u32_e64 v86, s[10:11], s24, v72
	s_waitcnt lgkmcnt(0)
	v_lshl_add_u64 v[0:1], s[34:35], 0, v[62:63]
	v_addc_co_u32_e64 v87, s[10:11], 0, v73, s[10:11]
	global_load_dwordx4 v[16:19], v[86:87], off
	v_add_co_u32_e64 v2, s[10:11], s25, v0
	s_nop 1
	v_addc_co_u32_e64 v3, s[10:11], 0, v1, s[10:11]
	v_add_co_u32_e64 v0, s[10:11], s26, v0
	global_load_dwordx4 v[78:81], v[2:3], off
	s_nop 0
	v_addc_co_u32_e64 v1, s[10:11], 0, v1, s[10:11]
	s_add_i32 s10, s5, s13
	s_ashr_i32 s11, s10, 31
	global_load_dwordx4 v[88:91], v[0:1], off offset:-4096
	global_load_dwordx4 v[102:105], v[0:1], off
	s_lshl_b64 s[10:11], s[10:11], 2
	s_add_u32 s10, s3, s10
	s_addc_u32 s11, s71, s11
	global_load_dwordx2 v[82:83], v58, s[10:11]
	global_load_dwordx4 v[106:109], v[2:3], off offset:-4096
	global_load_dwordx4 v[74:77], v[26:27], off
	global_load_dwordx4 v[110:113], v[24:25], off
	global_load_dwordx4 v[114:117], v[24:25], off offset:16
	global_load_dwordx4 v[118:121], v[26:27], off offset:16
	global_load_dwordx4 v[12:15], v[24:25], off offset:2064
	global_load_dwordx4 v[122:125], v[24:25], off offset:2048
	v_lshl_add_u64 v[0:1], s[34:35], 0, v[64:65]
	v_add_co_u32_e64 v4, s[10:11], s25, v0
	s_waitcnt vmcnt(11)
	v_lshlrev_b32_e32 v59, 16, v16
	v_addc_co_u32_e64 v5, s[10:11], 0, v1, s[10:11]
	v_add_co_u32_e64 v84, s[10:11], s26, v0
	v_and_b32_e32 v101, 0xffff0000, v16
	s_nop 0
	v_addc_co_u32_e64 v85, s[10:11], 0, v1, s[10:11]
	global_load_dwordx4 v[130:133], v[86:87], off offset:1024
	global_load_dwordx4 v[8:11], v[4:5], off offset:-4096
	global_load_dwordx4 v[0:3], v[4:5], off
	s_nop 0
	global_load_dwordx4 v[4:7], v[84:85], off offset:-4096
	v_lshlrev_b32_e32 v134, 16, v17
	v_and_b32_e32 v135, 0xffff0000, v17
	s_waitcnt vmcnt(11)
	v_sub_f32_e32 v135, v135, v82
	v_sub_f32_e32 v134, v134, v82
	v_sub_f32_e32 v137, v101, v82
	v_sub_f32_e32 v136, v59, v82
	v_pk_mul_f32 v[136:137], v[82:83], v[136:137] op_sel:[1,0]
	v_pk_mul_f32 v[134:135], v[82:83], v[134:135] op_sel:[1,0]
	s_waitcnt vmcnt(10)
	v_lshlrev_b32_e32 v142, 16, v106
	v_and_b32_e32 v143, 0xffff0000, v106
	v_lshlrev_b32_e32 v106, 16, v107
	v_and_b32_e32 v107, 0xffff0000, v107
	s_waitcnt vmcnt(8)
	v_pk_fma_f32 v[76:77], v[112:113], v[134:135], v[76:77]
	v_pk_fma_f32 v[74:75], v[110:111], v[136:137], v[74:75]
	v_lshlrev_b32_e32 v16, 16, v78
	v_and_b32_e32 v17, 0xffff0000, v78
	v_lshlrev_b32_e32 v78, 16, v79
	v_and_b32_e32 v79, 0xffff0000, v79
	v_pk_fma_f32 v[74:75], v[74:75], s[14:15], v[142:143] op_sel_hi:[1,0,1]
	v_pk_fma_f32 v[76:77], v[76:77], s[14:15], v[106:107] op_sel_hi:[1,0,1]
	v_lshlrev_b32_e32 v140, 16, v18
	v_and_b32_e32 v141, 0xffff0000, v18
	v_lshlrev_b32_e32 v138, 16, v19
	v_and_b32_e32 v139, 0xffff0000, v19
	v_lshlrev_b32_e32 v18, 16, v88
	v_and_b32_e32 v19, 0xffff0000, v88
	v_lshlrev_b32_e32 v88, 16, v89
	v_and_b32_e32 v89, 0xffff0000, v89
	v_pk_add_f32 v[16:17], v[74:75], v[16:17]
	v_pk_add_f32 v[74:75], v[76:77], v[78:79]
	v_lshlrev_b32_e32 v92, 16, v102
	v_and_b32_e32 v93, 0xffff0000, v102
	v_lshlrev_b32_e32 v102, 16, v103
	v_pk_add_f32 v[16:17], v[16:17], v[18:19]
	v_pk_add_f32 v[18:19], v[74:75], v[88:89]
	v_and_b32_e32 v103, 0xffff0000, v103
	v_pk_add_f32 v[74:75], v[16:17], v[92:93]
	v_pk_add_f32 v[76:77], v[18:19], v[102:103]
	global_load_dwordx4 v[16:19], v[84:85], off
	v_sub_f32_e32 v141, v141, v82
	v_sub_f32_e32 v140, v140, v82
	v_pk_mul_f32 v[140:141], v[82:83], v[140:141] op_sel:[1,0]
	v_lshlrev_b32_e32 v78, 16, v108
	s_waitcnt vmcnt(7)
	v_pk_fma_f32 v[112:113], v[114:115], v[140:141], v[118:119]
	v_and_b32_e32 v79, 0xffff0000, v108
	v_pk_fma_f32 v[78:79], v[112:113], s[14:15], v[78:79] op_sel_hi:[1,0,1]
	v_lshlrev_b32_e32 v84, 16, v80
	v_and_b32_e32 v85, 0xffff0000, v80
	v_sub_f32_e32 v139, v139, v82
	v_sub_f32_e32 v138, v138, v82
	v_pk_add_f32 v[78:79], v[78:79], v[84:85]
	v_lshlrev_b32_e32 v84, 16, v90
	v_and_b32_e32 v85, 0xffff0000, v90
	v_pk_mul_f32 v[138:139], v[82:83], v[138:139] op_sel:[1,0]
	v_pk_add_f32 v[78:79], v[78:79], v[84:85]
	v_lshlrev_b32_e32 v84, 16, v104
	v_and_b32_e32 v85, 0xffff0000, v104
	v_pk_fma_f32 v[110:111], v[116:117], v[138:139], v[120:121]
	v_pk_add_f32 v[78:79], v[78:79], v[84:85]
	v_lshlrev_b32_e32 v84, 16, v109
	v_and_b32_e32 v85, 0xffff0000, v109
	v_pk_fma_f32 v[84:85], v[110:111], s[14:15], v[84:85] op_sel_hi:[1,0,1]
	v_lshlrev_b32_e32 v80, 16, v81
	v_and_b32_e32 v81, 0xffff0000, v81
	v_pk_add_f32 v[80:81], v[84:85], v[80:81]
	v_lshlrev_b32_e32 v84, 16, v91
	v_and_b32_e32 v85, 0xffff0000, v91
	v_pk_add_f32 v[80:81], v[80:81], v[84:85]
	v_lshlrev_b32_e32 v84, 16, v105
	v_and_b32_e32 v85, 0xffff0000, v105
	v_pk_add_f32 v[80:81], v[80:81], v[84:85]
	v_mov_b32_e32 v84, v78
	v_mov_b32_e32 v85, v74
	v_mov_b32_e32 v88, v79
	v_mov_b32_e32 v89, v75
	v_pk_add_f32 v[84:85], v[84:85], v[88:89]
	v_mov_b32_e32 v88, v80
	v_mov_b32_e32 v89, v76
	v_mov_b32_e32 v90, v81
	v_mov_b32_e32 v91, v77
	v_pk_add_f32 v[88:89], v[88:89], v[90:91]
	s_waitcnt vmcnt(4)
	v_lshlrev_b32_e32 v59, 16, v130
	v_pk_add_f32 v[84:85], v[84:85], v[88:89]
	v_sub_f32_e32 v90, v59, v82
	v_pk_add_f32 v[88:89], v[84:85], v[84:85] op_sel:[0,1] op_sel_hi:[1,0]
	v_lshlrev_b32_e32 v84, 16, v131
	v_and_b32_e32 v89, 0xffff0000, v130
	v_and_b32_e32 v85, 0xffff0000, v131
	v_sub_f32_e32 v85, v85, v82
	v_sub_f32_e32 v84, v84, v82
	v_sub_f32_e32 v91, v89, v82
	v_lshlrev_b32_e32 v101, 16, v132
	v_and_b32_e32 v102, 0xffff0000, v132
	v_lshlrev_b32_e32 v103, 16, v133
	v_pk_mul_f32 v[90:91], v[82:83], v[90:91] op_sel:[1,0]
	v_pk_mul_f32 v[84:85], v[82:83], v[84:85] op_sel:[1,0]
	v_and_b32_e32 v104, 0xffff0000, v133
	v_pk_fma_f32 v[92:93], v[124:125], v[84:85], v[150:151]
	v_pk_fma_f32 v[84:85], v[122:123], v[90:91], v[148:149]
	v_sub_f32_e32 v90, v103, v82
	v_sub_f32_e32 v103, v102, v82
	v_sub_f32_e32 v102, v101, v82
	v_sub_f32_e32 v91, v104, v82
	v_pk_mul_f32 v[106:107], v[82:83], v[102:103] op_sel:[1,0]
	global_load_dwordx4 v[102:105], v[86:87], off offset:2048
	v_pk_fma_f32 v[122:123], v[12:13], v[106:107], v[144:145]
	v_pk_mul_f32 v[90:91], v[82:83], v[90:91] op_sel:[1,0]
	s_waitcnt vmcnt(4)
; DI float bflo(unsigned w) { return __uint_as_float(w << 16); }
; DI float bfhi(unsigned w) { return __uint_as_float(w & 0xffff0000u); }
; DI void p7_ln2(const Ctx& c) {
;     ...
;         for (int i = 0; i < 4; ++i) { const int d = (i * 64 + lane) * 8; const u32x4 yr = *(const u32x4*)(y1 + (size_t)tok * D + d);
;             const f32x4 y0 = {bflo(yr.x), bfhi(yr.x), bflo(yr.y), bfhi(yr.y)}, y1v = {bflo(yr.z), bfhi(yr.z), bflo(yr.w), bfhi(yr.w)};
;             const f32x4 g0 = *(const f32x4*)(l1w + d), g1 = *(const f32x4*)(l1w + d + 4), b0 = *(const f32x4*)(l1b + d), b1 = *(const f32x4*)(l1b + d + 4);
;             f32x4 a0 = ((y0 - mean1) * rstd1 * g0 + b0) * DN_ALPHA, a1 = ((y1v - mean1) * rstd1 * g1 + b1) * DN_ALPHA;
; #pragma unroll
;             for (int k = 0; k < 4; ++k) { const u32x4 v = *(const u32x4*)(yb + ((size_t)tok * 4 + k) * D + d);
;                 a0[0] += bflo(v.x); a0[1] += bfhi(v.x); a0[2] += bflo(v.y); a0[3] += bfhi(v.y); a1[0] += bflo(v.z); a1[1] += bfhi(v.z); a1[2] += bflo(v.w); a1[3] += bfhi(v.w); }
;             z[2 * i] = a0; z[2 * i + 1] = a1; s += ((a0[0] + a0[1]) + (a0[2] + a0[3])) + ((a1[0] + a1[1]) + (a1[2] + a1[3])); }
	v_lshlrev_b32_e32 v12, 16, v8
	v_and_b32_e32 v13, 0xffff0000, v8
	v_lshlrev_b32_e32 v8, 16, v9
	v_and_b32_e32 v9, 0xffff0000, v9
	v_pk_fma_f32 v[90:91], v[14:15], v[90:91], v[146:147]
	v_pk_fma_f32 v[12:13], v[84:85], s[14:15], v[12:13] op_sel_hi:[1,0,1]
	s_waitcnt vmcnt(3)
	v_lshlrev_b32_e32 v14, 16, v0
	v_and_b32_e32 v15, 0xffff0000, v0
	v_pk_fma_f32 v[8:9], v[92:93], s[14:15], v[8:9] op_sel_hi:[1,0,1]
	v_lshlrev_b32_e32 v0, 16, v1
	v_and_b32_e32 v1, 0xffff0000, v1
	v_pk_add_f32 v[12:13], v[12:13], v[14:15]
	s_waitcnt vmcnt(2)
	v_lshlrev_b32_e32 v14, 16, v4
	v_and_b32_e32 v15, 0xffff0000, v4
	v_pk_add_f32 v[0:1], v[8:9], v[0:1]
	v_lshlrev_b32_e32 v4, 16, v5
	v_and_b32_e32 v5, 0xffff0000, v5
	v_lshl_add_u64 v[124:125], s[34:35], 0, v[66:67]
	v_pk_add_f32 v[0:1], v[0:1], v[4:5]
	s_waitcnt vmcnt(1)
	v_lshlrev_b32_e32 v4, 16, v17
	v_and_b32_e32 v5, 0xffff0000, v17
	v_add_co_u32_e64 v22, s[10:11], s25, v124
	v_pk_add_f32 v[0:1], v[0:1], v[4:5]
	v_lshlrev_b32_e32 v4, 16, v10
	v_and_b32_e32 v5, 0xffff0000, v10
	v_addc_co_u32_e64 v23, s[10:11], 0, v125, s[10:11]
	v_pk_fma_f32 v[4:5], v[122:123], s[14:15], v[4:5] op_sel_hi:[1,0,1]
	v_lshlrev_b32_e32 v8, 16, v2
	v_and_b32_e32 v9, 0xffff0000, v2
	v_pk_add_f32 v[4:5], v[4:5], v[8:9]
	v_add_co_u32_e64 v8, s[10:11], s26, v124
	v_lshlrev_b32_e32 v84, 16, v16
	v_and_b32_e32 v85, 0xffff0000, v16
	v_addc_co_u32_e64 v9, s[10:11], 0, v125, s[10:11]
	v_lshlrev_b32_e32 v16, 16, v6
	v_and_b32_e32 v17, 0xffff0000, v6
	global_load_dwordx4 v[122:125], v[8:9], off offset:-4096
	global_load_dwordx4 v[126:129], v[8:9], off
	v_pk_add_f32 v[4:5], v[4:5], v[16:17]
	v_lshlrev_b32_e32 v8, 16, v18
	v_and_b32_e32 v9, 0xffff0000, v18
	v_pk_add_f32 v[4:5], v[4:5], v[8:9]
	v_lshlrev_b32_e32 v8, 16, v11
	v_and_b32_e32 v9, 0xffff0000, v11
	v_pk_fma_f32 v[8:9], v[90:91], s[14:15], v[8:9] op_sel_hi:[1,0,1]
	v_lshlrev_b32_e32 v2, 16, v3
	v_and_b32_e32 v3, 0xffff0000, v3
	v_pk_add_f32 v[20:21], v[12:13], v[14:15]
	global_load_dwordx4 v[12:15], v[22:23], off offset:-4096
	v_pk_add_f32 v[2:3], v[8:9], v[2:3]
	v_lshlrev_b32_e32 v6, 16, v7
	v_and_b32_e32 v7, 0xffff0000, v7
	v_pk_add_f32 v[84:85], v[20:21], v[84:85]
	v_pk_add_f32 v[2:3], v[2:3], v[6:7]
	v_lshlrev_b32_e32 v6, 16, v19
	v_and_b32_e32 v7, 0xffff0000, v19
	global_load_dwordx4 v[16:19], v[86:87], off offset:3072
	v_pk_add_f32 v[2:3], v[2:3], v[6:7]
	global_load_dwordx4 v[20:23], v[22:23], off
	v_mov_b32_e32 v6, v84
	v_mov_b32_e32 v7, v0
	v_mov_b32_e32 v8, v85
	v_mov_b32_e32 v9, v1
	v_pk_add_f32 v[6:7], v[6:7], v[8:9]
	v_mov_b32_e32 v8, v5
	v_pk_add_f32 v[90:91], v[6:7], v[6:7] op_sel:[0,1] op_sel_hi:[1,0]
	v_mov_b32_e32 v6, v4
	v_mov_b32_e32 v7, v2
	v_mov_b32_e32 v9, v3
	v_pk_add_f32 v[6:7], v[6:7], v[8:9]
	v_lshl_add_u64 v[134:135], s[34:35], 0, v[68:69]
	v_pk_add_f32 v[92:93], v[6:7], v[6:7] op_sel:[0,1] op_sel_hi:[1,0]
	s_waitcnt vmcnt(5)
	v_lshlrev_b32_e32 v8, 16, v102
	v_and_b32_e32 v9, 0xffff0000, v102
	v_lshlrev_b32_e32 v6, 16, v103
	v_and_b32_e32 v7, 0xffff0000, v103
	v_sub_f32_e32 v7, v7, v82
	v_sub_f32_e32 v6, v6, v82
	v_sub_f32_e32 v9, v9, v82
	v_sub_f32_e32 v8, v8, v82
	v_lshlrev_b32_e32 v59, 16, v104
	v_and_b32_e32 v86, 0xffff0000, v104
	v_lshlrev_b32_e32 v87, 16, v105
	v_and_b32_e32 v89, 0xffff0000, v105
	v_pk_mul_f32 v[8:9], v[82:83], v[8:9] op_sel:[1,0]
	v_pk_mul_f32 v[6:7], v[82:83], v[6:7] op_sel:[1,0]
	v_add_co_u32_e64 v130, s[10:11], s25, v134
	s_waitcnt vmcnt(5)
	v_pk_fma_f32 v[10:11], v[158:159], v[6:7], v[166:167]
	v_pk_fma_f32 v[6:7], v[156:157], v[8:9], v[164:165]
	v_sub_f32_e32 v9, v89, v82
	v_sub_f32_e32 v8, v87, v82
	v_sub_f32_e32 v87, v86, v82
	v_sub_f32_e32 v86, v59, v82
	v_pk_mul_f32 v[86:87], v[82:83], v[86:87] op_sel:[1,0]
	v_pk_mul_f32 v[8:9], v[82:83], v[8:9] op_sel:[1,0]
	v_pk_fma_f32 v[86:87], v[152:153], v[86:87], v[160:161]
	v_pk_fma_f32 v[142:143], v[154:155], v[8:9], v[162:163]
	v_addc_co_u32_e64 v131, s[10:11], 0, v135, s[10:11]
	v_add_co_u32_e64 v138, s[10:11], s26, v134
	global_load_dwordx4 v[118:121], v[130:131], off offset:-4096
	s_nop 0
	global_load_dwordx4 v[130:133], v[130:131], off
	v_addc_co_u32_e64 v139, s[10:11], 0, v135, s[10:11]
	global_load_dwordx4 v[134:137], v[138:139], off offset:-4096
	s_waitcnt vmcnt(5)
	v_lshlrev_b32_e32 v8, 16, v12
	global_load_dwordx4 v[138:141], v[138:139], off
	v_and_b32_e32 v9, 0xffff0000, v12
	v_pk_fma_f32 v[6:7], v[6:7], s[14:15], v[8:9] op_sel_hi:[1,0,1]
	s_waitcnt vmcnt(5)
	v_lshlrev_b32_e32 v59, 16, v19
	s_waitcnt vmcnt(4)
	v_lshlrev_b32_e32 v8, 16, v20
	v_and_b32_e32 v9, 0xffff0000, v20
	v_pk_add_f32 v[6:7], v[6:7], v[8:9]
	v_lshlrev_b32_e32 v8, 16, v122
	v_and_b32_e32 v9, 0xffff0000, v122
	v_pk_add_f32 v[6:7], v[6:7], v[8:9]
	v_lshlrev_b32_e32 v8, 16, v126
	v_and_b32_e32 v9, 0xffff0000, v126
	v_pk_add_f32 v[6:7], v[6:7], v[8:9]
	v_lshlrev_b32_e32 v8, 16, v13
	v_and_b32_e32 v9, 0xffff0000, v13
	v_pk_fma_f32 v[8:9], v[10:11], s[14:15], v[8:9] op_sel_hi:[1,0,1]
	v_lshlrev_b32_e32 v10, 16, v21
	v_and_b32_e32 v11, 0xffff0000, v21
	v_pk_add_f32 v[8:9], v[8:9], v[10:11]
	v_lshlrev_b32_e32 v10, 16, v123
	v_and_b32_e32 v11, 0xffff0000, v123
	v_pk_add_f32 v[8:9], v[8:9], v[10:11]
	v_lshlrev_b32_e32 v10, 16, v127
	v_and_b32_e32 v11, 0xffff0000, v127
	v_pk_add_f32 v[8:9], v[8:9], v[10:11]
	v_lshlrev_b32_e32 v10, 16, v14
	v_and_b32_e32 v11, 0xffff0000, v14
	v_pk_fma_f32 v[10:11], v[86:87], s[14:15], v[10:11] op_sel_hi:[1,0,1]
	v_lshlrev_b32_e32 v12, 16, v22
	v_and_b32_e32 v13, 0xffff0000, v22
	v_pk_add_f32 v[10:11], v[10:11], v[12:13]
	v_lshlrev_b32_e32 v12, 16, v124
	v_and_b32_e32 v13, 0xffff0000, v124
	v_pk_add_f32 v[10:11], v[10:11], v[12:13]
	v_lshlrev_b32_e32 v12, 16, v128
	v_and_b32_e32 v13, 0xffff0000, v128
	v_pk_add_f32 v[10:11], v[10:11], v[12:13]
	v_lshlrev_b32_e32 v12, 16, v15
	v_and_b32_e32 v13, 0xffff0000, v15
	v_pk_fma_f32 v[12:13], v[142:143], s[14:15], v[12:13] op_sel_hi:[1,0,1]
	v_lshlrev_b32_e32 v14, 16, v23
	v_and_b32_e32 v15, 0xffff0000, v23
	v_pk_add_f32 v[12:13], v[12:13], v[14:15]
	v_lshlrev_b32_e32 v14, 16, v125
	v_and_b32_e32 v15, 0xffff0000, v125
	v_pk_add_f32 v[12:13], v[12:13], v[14:15]
	v_lshlrev_b32_e32 v14, 16, v129
	v_and_b32_e32 v15, 0xffff0000, v129
	v_pk_add_f32 v[12:13], v[12:13], v[14:15]
	v_lshlrev_b32_e32 v20, 16, v16
	v_and_b32_e32 v16, 0xffff0000, v16
	v_lshlrev_b32_e32 v14, 16, v17
	v_and_b32_e32 v15, 0xffff0000, v17
	v_pk_add_f32 v[86:87], v[8:9], v[8:9] op_sel:[0,1] op_sel_hi:[1,0]
	v_sub_f32_e32 v15, v15, v82
	v_sub_f32_e32 v14, v14, v82
	v_sub_f32_e32 v17, v16, v82
	v_sub_f32_e32 v16, v20, v82
	v_pk_add_f32 v[22:23], v[6:7], v[6:7] op_sel:[0,1] op_sel_hi:[1,0]
	v_and_b32_e32 v87, 0xffff0000, v19
	v_pk_mul_f32 v[16:17], v[82:83], v[16:17] op_sel:[1,0]
	v_pk_mul_f32 v[14:15], v[82:83], v[14:15] op_sel:[1,0]
	v_lshlrev_b32_e32 v23, 16, v18
	v_and_b32_e32 v21, 0xffff0000, v18
	s_waitcnt vmcnt(4)
; DI float bflo(unsigned w) { return __uint_as_float(w << 16); }
; DI float bfhi(unsigned w) { return __uint_as_float(w & 0xffff0000u); }
; DI void p7_ln2(const Ctx& c) {
;     ...
;             for (int k = 0; k < 4; ++k) { const u32x4 v = *(const u32x4*)(yb + ((size_t)tok * 4 + k) * D + d);
;                 a0[0] += bflo(v.x); a0[1] += bfhi(v.x); a0[2] += bflo(v.y); a0[3] += bfhi(v.y); a1[0] += bflo(v.z); a1[1] += bfhi(v.z); a1[2] += bflo(v.w); a1[3] += bfhi(v.w); }
;             z[2 * i] = a0; z[2 * i + 1] = a1; s += ((a0[0] + a0[1]) + (a0[2] + a0[3])) + ((a1[0] + a1[1]) + (a1[2] + a1[3])); }
; #pragma unroll
;         for (int o = 32; o >= 1; o >>= 1) s += __shfl_xor(s, o);
;         const float mean = s * (1.0f / D); float qv = 0.f;
; #pragma unroll
;         for (int i = 0; i < 8; ++i) { const f32x4 dl = z[i] - mean; qv += (dl[0] * dl[0] + dl[1] * dl[1]) + (dl[2] * dl[2] + dl[3] * dl[3]); }
; #pragma unroll
;         for (int o = 32; o >= 1; o >>= 1) qv += __shfl_xor(qv, o);
	v_pk_fma_f32 v[18:19], v[174:175], v[14:15], v[182:183]
	v_pk_fma_f32 v[14:15], v[172:173], v[16:17], v[180:181]
	v_sub_f32_e32 v17, v87, v82
	v_sub_f32_e32 v16, v59, v82
	v_sub_f32_e32 v21, v21, v82
	v_sub_f32_e32 v20, v23, v82
	v_pk_mul_f32 v[16:17], v[82:83], v[16:17] op_sel:[1,0]
	v_pk_mul_f32 v[20:21], v[82:83], v[20:21] op_sel:[1,0]
	v_pk_fma_f32 v[82:83], v[170:171], v[16:17], v[178:179]
	s_waitcnt vmcnt(3)
	v_lshlrev_b32_e32 v16, 16, v118
	v_and_b32_e32 v17, 0xffff0000, v118
	v_pk_fma_f32 v[14:15], v[14:15], s[14:15], v[16:17] op_sel_hi:[1,0,1]
	s_waitcnt vmcnt(2)
	v_lshlrev_b32_e32 v16, 16, v130
	v_and_b32_e32 v17, 0xffff0000, v130
	v_pk_add_f32 v[14:15], v[14:15], v[16:17]
	s_waitcnt vmcnt(1)
	v_lshlrev_b32_e32 v16, 16, v134
	v_and_b32_e32 v17, 0xffff0000, v134
	v_pk_add_f32 v[14:15], v[14:15], v[16:17]
	s_waitcnt vmcnt(0)
	v_lshlrev_b32_e32 v16, 16, v138
	v_and_b32_e32 v17, 0xffff0000, v138
	v_pk_add_f32 v[14:15], v[14:15], v[16:17]
	v_lshlrev_b32_e32 v16, 16, v119
	v_and_b32_e32 v17, 0xffff0000, v119
	v_pk_fma_f32 v[16:17], v[18:19], s[14:15], v[16:17] op_sel_hi:[1,0,1]
	v_lshlrev_b32_e32 v18, 16, v131
	v_and_b32_e32 v19, 0xffff0000, v131
	v_pk_add_f32 v[16:17], v[16:17], v[18:19]
	v_lshlrev_b32_e32 v18, 16, v135
	v_and_b32_e32 v19, 0xffff0000, v135
	v_pk_add_f32 v[16:17], v[16:17], v[18:19]
	v_lshlrev_b32_e32 v18, 16, v139
	v_and_b32_e32 v19, 0xffff0000, v139
	v_pk_fma_f32 v[20:21], v[168:169], v[20:21], v[176:177]
	v_pk_add_f32 v[16:17], v[16:17], v[18:19]
	v_lshlrev_b32_e32 v18, 16, v120
	v_and_b32_e32 v19, 0xffff0000, v120
	v_pk_fma_f32 v[18:19], v[20:21], s[14:15], v[18:19] op_sel_hi:[1,0,1]
	v_lshlrev_b32_e32 v20, 16, v132
	v_and_b32_e32 v21, 0xffff0000, v132
	v_pk_add_f32 v[18:19], v[18:19], v[20:21]
	v_lshlrev_b32_e32 v20, 16, v136
	v_and_b32_e32 v21, 0xffff0000, v136
	v_pk_add_f32 v[18:19], v[18:19], v[20:21]
	v_lshlrev_b32_e32 v20, 16, v140
	v_and_b32_e32 v21, 0xffff0000, v140
	v_pk_add_f32 v[18:19], v[18:19], v[20:21]
	v_lshlrev_b32_e32 v20, 16, v121
	v_and_b32_e32 v21, 0xffff0000, v121
	v_pk_fma_f32 v[20:21], v[82:83], s[14:15], v[20:21] op_sel_hi:[1,0,1]
	v_lshlrev_b32_e32 v82, 16, v133
	v_and_b32_e32 v83, 0xffff0000, v133
	v_pk_add_f32 v[20:21], v[20:21], v[82:83]
	v_lshlrev_b32_e32 v82, 16, v137
	v_and_b32_e32 v83, 0xffff0000, v137
	v_pk_add_f32 v[122:123], v[10:11], v[10:11] op_sel:[0,1] op_sel_hi:[1,0]
	v_pk_add_f32 v[124:125], v[12:13], v[12:13] op_sel:[0,1] op_sel_hi:[1,0]
	v_pk_add_f32 v[20:21], v[20:21], v[82:83]
	v_lshlrev_b32_e32 v82, 16, v141
	v_and_b32_e32 v83, 0xffff0000, v141
	v_pk_add_f32 v[20:21], v[20:21], v[82:83]
	v_mov_b32_e32 v123, v14
	v_mov_b32_e32 v125, v15
	v_mov_b32_e32 v23, v16
	v_mov_b32_e32 v87, v17
	v_pk_add_f32 v[82:83], v[122:123], v[124:125]
	v_pk_add_f32 v[22:23], v[22:23], v[86:87]
	v_mov_b32_e32 v89, v18
	v_mov_b32_e32 v59, v19
	v_mov_b32_e32 v93, v20
	v_mov_b32_e32 v91, v21
	v_pk_add_f32 v[22:23], v[82:83], v[22:23]
	v_pk_add_f32 v[82:83], v[88:89], v[58:59]
	v_pk_add_f32 v[86:87], v[92:93], v[90:91]
	s_nop 0
	v_pk_add_f32 v[82:83], v[82:83], v[86:87]
	s_nop 0
	v_pk_add_f32 v[22:23], v[82:83], v[22:23]
	s_nop 0
	v_add_f32_e32 v22, v22, v23
	ds_bpermute_b32 v23, v94, v22
	s_waitcnt lgkmcnt(0)
	v_add_f32_e32 v22, v22, v23
	ds_bpermute_b32 v23, v95, v22
	s_waitcnt lgkmcnt(0)
	v_add_f32_e32 v22, v22, v23
	ds_bpermute_b32 v23, v96, v22
	s_waitcnt lgkmcnt(0)
	v_add_f32_e32 v22, v22, v23
	ds_bpermute_b32 v23, v97, v22
	s_waitcnt lgkmcnt(0)
	v_add_f32_e32 v22, v22, v23
	ds_bpermute_b32 v23, v98, v22
	s_waitcnt lgkmcnt(0)
	v_add_f32_e32 v22, v22, v23
	ds_bpermute_b32 v23, v99, v22
	s_waitcnt lgkmcnt(0)
	v_add_f32_e32 v59, v22, v23
	v_fmamk_f32 v75, v59, 0xba000000, v75
	v_fmamk_f32 v79, v59, 0xba000000, v79
	v_fmamk_f32 v77, v59, 0xba000000, v77
	v_fmac_f32_e32 v74, 0xba000000, v59
	v_fmamk_f32 v81, v59, 0xba000000, v81
	v_fmac_f32_e32 v78, 0xba000000, v59
	v_mov_b32_e32 v82, v75
	v_mov_b32_e32 v83, v79
	v_fmac_f32_e32 v76, 0xba000000, v59
	v_fmac_f32_e32 v80, 0xba000000, v59
	v_mov_b32_e32 v22, v74
	v_mov_b32_e32 v23, v78
	v_pk_mul_f32 v[82:83], v[82:83], v[82:83]
	v_mov_b32_e32 v86, v77
	v_mov_b32_e32 v87, v81
	v_pk_fma_f32 v[22:23], v[22:23], v[22:23], v[82:83]
	v_mov_b32_e32 v82, v76
	v_mov_b32_e32 v83, v80
	v_pk_mul_f32 v[86:87], v[86:87], v[86:87]
	v_fmamk_f32 v85, v59, 0xba000000, v85
	v_pk_fma_f32 v[82:83], v[82:83], v[82:83], v[86:87]
	v_fmac_f32_e32 v84, 0xba000000, v59
	v_pk_add_f32 v[22:23], v[22:23], v[82:83]
	v_fmamk_f32 v1, v59, 0xba000000, v1
	v_fmac_f32_e32 v0, 0xba000000, v59
	v_pk_add_f32 v[22:23], v[22:23], v[22:23] op_sel_hi:[0,1]
	v_pk_mul_f32 v[82:83], v[0:1], v[0:1]
	v_pk_mul_f32 v[86:87], v[84:85], v[84:85]
	v_fmac_f32_e32 v4, 0xba000000, v59
	v_pk_mov_b32 v[88:89], v[86:87], v[82:83] op_sel:[1,0]
	v_mov_b32_e32 v87, v83
	v_fmamk_f32 v5, v59, 0xba000000, v5
	v_fmac_f32_e32 v2, 0xba000000, v59
	v_mul_f32_e32 v22, v4, v4
	v_pk_add_f32 v[82:83], v[88:89], v[86:87]
	v_fmamk_f32 v3, v59, 0xba000000, v3
	v_pk_fma_f32 v[86:87], v[4:5], v[4:5], v[22:23] op_sel_hi:[1,1,0]
	v_mul_f32_e32 v22, v2, v2
	v_pk_add_f32 v[82:83], v[82:83], v[82:83] op_sel_hi:[0,1]
	v_pk_fma_f32 v[88:89], v[2:3], v[2:3], v[22:23] op_sel_hi:[1,1,0]
	v_fmamk_f32 v9, v59, 0xba000000, v9
	v_fmac_f32_e32 v8, 0xba000000, v59
	v_fmamk_f32 v7, v59, 0xba000000, v7
	v_fmac_f32_e32 v6, 0xba000000, v59
	v_mul_f32_e32 v86, v6, v6
	v_mul_f32_e32 v88, v7, v7
	v_mul_f32_e32 v82, v8, v8
	v_mul_f32_e32 v22, v9, v9
	v_pk_add_f32 v[86:87], v[86:87], v[88:89]
	v_pk_add_f32 v[22:23], v[82:83], v[22:23]
	v_fmamk_f32 v11, v59, 0xba000000, v11
	v_pk_add_f32 v[22:23], v[86:87], v[22:23]
	v_fmac_f32_e32 v10, 0xba000000, v59
	v_fmamk_f32 v13, v59, 0xba000000, v13
	v_fmac_f32_e32 v12, 0xba000000, v59
	v_pk_add_f32 v[22:23], v[22:23], v[22:23] op_sel_hi:[0,1]
	v_pk_mul_f32 v[82:83], v[12:13], v[12:13]
	v_pk_mul_f32 v[110:111], v[10:11], v[10:11]
	v_fmac_f32_e32 v14, 0xba000000, v59
	v_pk_mov_b32 v[112:113], v[110:111], v[82:83] op_sel:[1,0]
	v_mov_b32_e32 v111, v83
	v_fmamk_f32 v15, v59, 0xba000000, v15
	v_fmac_f32_e32 v16, 0xba000000, v59
	v_mul_f32_e32 v22, v14, v14
	v_pk_add_f32 v[82:83], v[112:113], v[110:111]
	v_fmamk_f32 v17, v59, 0xba000000, v17
	v_pk_fma_f32 v[110:111], v[14:15], v[14:15], v[22:23] op_sel_hi:[1,1,0]
	v_mul_f32_e32 v22, v16, v16
	v_pk_add_f32 v[82:83], v[82:83], v[82:83] op_sel_hi:[0,1]
	v_pk_fma_f32 v[112:113], v[16:17], v[16:17], v[22:23] op_sel_hi:[1,1,0]
	v_fmamk_f32 v21, v59, 0xba000000, v21
	v_fmac_f32_e32 v20, 0xba000000, v59
	v_fmamk_f32 v19, v59, 0xba000000, v19
	v_fmac_f32_e32 v18, 0xba000000, v59
	v_mul_f32_e32 v110, v18, v18
	v_mul_f32_e32 v112, v19, v19
	v_mul_f32_e32 v82, v20, v20
	v_mul_f32_e32 v22, v21, v21
	v_pk_add_f32 v[110:111], v[110:111], v[112:113]
	v_pk_add_f32 v[22:23], v[82:83], v[22:23]
	s_nop 0
	v_pk_add_f32 v[22:23], v[110:111], v[22:23]
	s_nop 0
	v_add_f32_e32 v22, v22, v23
	ds_bpermute_b32 v23, v94, v22
	s_waitcnt lgkmcnt(0)
; DI u32x2 pack4(f32x4 v) { bf16x4_t r = __builtin_convertvector(v, bf16x4_t); return __builtin_bit_cast(u32x2, r); }
; DI void p7_ln2(const Ctx& c) {
;     ...
;         for (int o = 32; o >= 1; o >>= 1) qv += __shfl_xor(qv, o);
;         const float rstd = rsqrtf(qv * (1.0f / D) + LN_EPS);
; #pragma unroll
;         for (int i = 0; i < 4; ++i) { const int d = (i * 64 + lane) * 8;
;             const f32x4 g0 = *(const f32x4*)(l2w + d), g1 = *(const f32x4*)(l2w + d + 4), b0 = *(const f32x4*)(l2b + d), b1 = *(const f32x4*)(l2b + d + 4);
;             const u32x2 lo = pack4((z[2 * i] - mean) * rstd * g0 + b0), hi = pack4((z[2 * i + 1] - mean) * rstd * g1 + b1);
;             *(u32x4*)(x2b + (size_t)tok * D + d) = (u32x4){lo.x, lo.y, hi.x, hi.y}; }
;         float q2 = (lane < 32) ? ssq[(size_t)tok * 32 + lane] : 0.f;
	v_add_f32_e32 v22, v22, v23
	ds_bpermute_b32 v23, v95, v22
	s_waitcnt lgkmcnt(0)
	v_add_f32_e32 v22, v22, v23
	ds_bpermute_b32 v23, v96, v22
	s_waitcnt lgkmcnt(0)
	v_add_f32_e32 v22, v22, v23
	ds_bpermute_b32 v23, v97, v22
	s_waitcnt lgkmcnt(0)
	v_add_f32_e32 v22, v22, v23
	ds_bpermute_b32 v23, v98, v22
	s_waitcnt lgkmcnt(0)
	v_add_f32_e32 v22, v22, v23
	ds_bpermute_b32 v23, v99, v22
	s_waitcnt lgkmcnt(0)
	v_add_f32_e32 v22, v22, v23
	v_fmamk_f32 v22, v22, 0x3a000000, v100
	v_mul_f32_e32 v23, 0x4b800000, v22
	v_cmp_gt_f32_e64 s[10:11], s27, v22
	s_nop 1
	v_cndmask_b32_e64 v22, v22, v23, s[10:11]
	v_rsq_f32_e32 v22, v22
	s_nop 0
	v_mul_f32_e32 v23, 0x45800000, v22
	v_cndmask_b32_e64 v22, v22, v23, s[10:11]
	v_pk_mul_f32 v[76:77], v[76:77], v[22:23] op_sel_hi:[1,0]
	v_pk_mul_f32 v[74:75], v[74:75], v[22:23] op_sel_hi:[1,0]
	v_pk_mul_f32 v[78:79], v[78:79], v[22:23] op_sel_hi:[1,0]
	s_waitcnt vmcnt(0)
	v_pk_fma_f32 v[82:83], v[188:189], v[74:75], v[196:197]
	v_pk_fma_f32 v[74:75], v[190:191], v[76:77], v[198:199]
	v_pk_mul_f32 v[76:77], v[80:81], v[22:23] op_sel_hi:[1,0]
	v_pk_fma_f32 v[78:79], v[184:185], v[78:79], v[192:193]
	v_pk_fma_f32 v[76:77], v[186:187], v[76:77], v[194:195]
	v_add_co_u32_e64 v90, s[10:11], s28, v72
	v_cvt_pk_bf16_f32 v75, v74, v75
	v_cvt_pk_bf16_f32 v74, v82, v83
	v_cvt_pk_bf16_f32 v77, v76, v77
	v_cvt_pk_bf16_f32 v76, v78, v79
	v_addc_co_u32_e64 v91, s[10:11], 0, v73, s[10:11]
	global_store_dwordx4 v[90:91], v[74:77], off sc1
	s_nop 0
	v_pk_mul_f32 v[84:85], v[84:85], v[22:23] op_sel_hi:[1,0]
	v_pk_mul_f32 v[0:1], v[0:1], v[22:23] op_sel_hi:[1,0]
	v_pk_mul_f32 v[4:5], v[4:5], v[22:23] op_sel_hi:[1,0]
	v_pk_mul_f32 v[2:3], v[2:3], v[22:23] op_sel_hi:[1,0]
	s_waitcnt vmcnt(1)
	v_pk_fma_f32 v[74:75], v[206:207], v[0:1], v[202:203]
	v_pk_fma_f32 v[0:1], v[204:205], v[84:85], v[200:201]
	s_waitcnt vmcnt(1)
	v_pk_fma_f32 v[72:73], v[210:211], v[2:3], v[218:219]
	v_pk_fma_f32 v[2:3], v[208:209], v[4:5], v[216:217]
	v_cvt_pk_bf16_f32 v0, v0, v1
	v_cvt_pk_bf16_f32 v1, v74, v75
	v_cvt_pk_bf16_f32 v2, v2, v3
	v_cvt_pk_bf16_f32 v3, v72, v73
	global_store_dwordx4 v[90:91], v[0:3], off offset:1024 sc1
	s_nop 0
	v_pk_mul_f32 v[4:5], v[6:7], v[22:23] op_sel_hi:[1,0]
	v_pk_mul_f32 v[6:7], v[8:9], v[22:23] op_sel_hi:[1,0]
	s_waitcnt vmcnt(2)
	v_pk_fma_f32 v[0:1], v[224:225], v[4:5], v[220:221]
	v_pk_fma_f32 v[2:3], v[226:227], v[6:7], v[222:223]
	v_cvt_pk_bf16_f32 v0, v0, v1
	v_cvt_pk_bf16_f32 v1, v2, v3
	v_pk_mul_f32 v[2:3], v[10:11], v[22:23] op_sel_hi:[1,0]
	v_pk_mul_f32 v[4:5], v[12:13], v[22:23] op_sel_hi:[1,0]
	s_waitcnt vmcnt(2)
	v_pk_fma_f32 v[2:3], v[230:231], v[2:3], v[234:235]
	v_pk_fma_f32 v[4:5], v[232:233], v[4:5], v[236:237]
	v_cvt_pk_bf16_f32 v2, v2, v3
	v_cvt_pk_bf16_f32 v3, v4, v5
	global_store_dwordx4 v[90:91], v[0:3], off offset:2048 sc1
	s_nop 0
	v_pk_mul_f32 v[12:13], v[14:15], v[22:23] op_sel_hi:[1,0]
	v_pk_mul_f32 v[14:15], v[16:17], v[22:23] op_sel_hi:[1,0]
	s_waitcnt vmcnt(3)
	v_pk_fma_f32 v[0:1], v[244:245], v[12:13], v[238:239]
	v_pk_fma_f32 v[2:3], v[246:247], v[14:15], v[240:241]
	v_cvt_pk_bf16_f32 v0, v0, v1
	v_cvt_pk_bf16_f32 v1, v2, v3
	v_pk_mul_f32 v[2:3], v[18:19], v[22:23] op_sel_hi:[1,0]
	v_pk_mul_f32 v[4:5], v[20:21], v[22:23] op_sel_hi:[1,0]
	s_waitcnt vmcnt(3)
	v_pk_fma_f32 v[2:3], v[248:249], v[2:3], v[252:253]
	v_pk_fma_f32 v[4:5], v[250:251], v[4:5], v[254:255]
	v_cvt_pk_bf16_f32 v2, v2, v3
	v_cvt_pk_bf16_f32 v3, v4, v5
	global_store_dwordx4 v[90:91], v[0:3], off offset:3072 sc1
	s_nop 1
	v_mov_b32_e32 v0, 0
	s_and_saveexec_b64 s[10:11], vcc
	s_cbranch_execz .LBB0_979
	v_lshl_add_u64 v[0:1], s[34:35], 0, v[60:61]
	global_load_dword v0, v[0:1], off
